# LN1 router logits as packed f32 FMAs (2 v_pk_fma per expert/quad, f32 accumulate, pair-sum at end) ; rwkv_out: two serialized gate loads per half hoisted into the first load batch
# speedup vs baseline: 1.0104x; 1.0104x over previous
; __device__ __forceinline__ void r4_zero_state(const Params& p, int l, unsigned char* ws, unsigned char* ob, int bh, int lane) {
;     ...
; #pragma unroll 1
;     for (int rb = 0; rb < 2; ++rb) {
;         unsigned short y0s[16], y1s[16], v0[16], v1[16], g0[16], g1[16]; float bcv[16];
; #pragma unroll
;         for (int r = 0; r < 16; ++r) { const int t = 32 * rb + (r & 3) + 8 * (r >> 2) + 4 * hi; const size_t row = (size_t)b * LT + t;
;             y0s[r] = YLg[TM(t, l31)]; y1s[r] = YLg[TM(t, 32 + l31)]; v0[r] = VVg[TM(t, l31)]; v1[r] = VVg[TM(t, 32 + l31)];
;             g0[r] = Gg[row * 256 + h * 64 + l31]; g1[r] = Gg[row * 256 + h * 64 + 32 + l31]; bcv[r] = BCg[row * 4 + h]; }
.LBB0_759:
	v_cndmask_b32_e64 v0, 0, 1, s[10:11]
	v_cmp_ne_u32_e32 vcc, 1, v0
	v_or_b32_e32 v0, s16, v75
	v_lshl_add_u64 v[36:37], s[6:7], 0, v[0:1]
	v_lshl_or_b32 v6, v0, 4, v76
	v_lshlrev_b32_e32 v85, 1, v6
	v_lshlrev_b64 v[6:7], 9, v[36:37]
	v_lshl_add_u64 v[38:39], v[2:3], 0, v[6:7]
	v_lshl_add_u64 v[6:7], v[36:37], 4, s[8:9]
	global_load_dword v84, v[6:7], off
	v_or_b32_e32 v6, 1, v0
	v_mov_b32_e32 v7, v1
	v_lshl_add_u64 v[34:35], s[6:7], 0, v[6:7]
	v_lshl_or_b32 v6, v6, 4, v76
	v_lshlrev_b32_e32 v88, 1, v6
	v_lshlrev_b64 v[6:7], 9, v[34:35]
	v_lshl_add_u64 v[40:41], v[2:3], 0, v[6:7]
	v_lshl_add_u64 v[6:7], v[34:35], 4, s[8:9]
	global_load_dword v129, v[6:7], off
	v_or_b32_e32 v6, 2, v0
	v_mov_b32_e32 v7, v1
	v_lshl_add_u64 v[32:33], s[6:7], 0, v[6:7]
	v_lshl_or_b32 v6, v6, 4, v76
	v_lshlrev_b32_e32 v90, 1, v6
	v_lshlrev_b64 v[6:7], 9, v[32:33]
	v_lshl_add_u64 v[42:43], v[2:3], 0, v[6:7]
	v_lshl_add_u64 v[6:7], v[32:33], 4, s[8:9]
	v_or_b32_e32 v68, s16, v74
	global_load_dword v122, v[6:7], off
	v_or_b32_e32 v6, 3, v68
	v_mov_b32_e32 v7, v1
	v_lshl_add_u64 v[30:31], s[6:7], 0, v[6:7]
	v_lshl_or_b32 v6, v6, 4, v76
	v_lshlrev_b32_e32 v92, 1, v6
	v_lshlrev_b64 v[6:7], 9, v[30:31]
	v_lshl_add_u64 v[44:45], v[2:3], 0, v[6:7]
	v_lshl_add_u64 v[6:7], v[30:31], 4, s[8:9]
	global_load_dword v118, v[6:7], off
	v_or_b32_e32 v6, 8, v0
	v_mov_b32_e32 v7, v1
	v_lshl_add_u64 v[28:29], s[6:7], 0, v[6:7]
	v_lshl_or_b32 v6, v6, 4, v76
	v_lshlrev_b32_e32 v95, 1, v6
	v_lshlrev_b64 v[6:7], 9, v[28:29]
	v_lshl_add_u64 v[46:47], v[2:3], 0, v[6:7]
	v_lshl_add_u64 v[6:7], v[28:29], 4, s[8:9]
	global_load_dword v114, v[6:7], off
	v_or_b32_e32 v6, 9, v0
	v_mov_b32_e32 v7, v1
	v_lshl_add_u64 v[26:27], s[6:7], 0, v[6:7]
	v_lshl_or_b32 v6, v6, 4, v76
	v_lshlrev_b32_e32 v97, 1, v6
	v_lshlrev_b64 v[6:7], 9, v[26:27]
	v_lshl_add_u64 v[48:49], v[2:3], 0, v[6:7]
	v_lshl_add_u64 v[6:7], v[26:27], 4, s[8:9]
	global_load_dword v107, v[6:7], off
	v_or_b32_e32 v6, 10, v0
	v_mov_b32_e32 v7, v1
	v_lshl_add_u64 v[24:25], s[6:7], 0, v[6:7]
	v_lshl_or_b32 v6, v6, 4, v76
	v_lshlrev_b32_e32 v99, 1, v6
	v_lshlrev_b64 v[6:7], 9, v[24:25]
	v_lshl_add_u64 v[50:51], v[2:3], 0, v[6:7]
	v_lshl_add_u64 v[6:7], v[24:25], 4, s[8:9]
	global_load_dword v100, v[6:7], off
	v_or_b32_e32 v6, 11, v68
	v_mov_b32_e32 v7, v1
	v_lshl_add_u64 v[22:23], s[6:7], 0, v[6:7]
	v_lshl_or_b32 v6, v6, 4, v76
	v_lshlrev_b32_e32 v102, 1, v6
	v_lshlrev_b64 v[6:7], 9, v[22:23]
	v_lshl_add_u64 v[52:53], v[2:3], 0, v[6:7]
	v_lshl_add_u64 v[6:7], v[22:23], 4, s[8:9]
	global_load_dword v93, v[6:7], off
	v_or_b32_e32 v6, 16, v0
	v_mov_b32_e32 v7, v1
	v_lshl_add_u64 v[20:21], s[6:7], 0, v[6:7]
	v_lshl_or_b32 v6, v6, 4, v76
	v_lshlrev_b32_e32 v104, 1, v6
	v_lshlrev_b64 v[6:7], 9, v[20:21]
	v_lshl_add_u64 v[54:55], v[2:3], 0, v[6:7]
	v_lshl_add_u64 v[6:7], v[20:21], 4, s[8:9]
	global_load_dword v86, v[6:7], off
	v_or_b32_e32 v6, 17, v0
	v_mov_b32_e32 v7, v1
	v_lshl_add_u64 v[18:19], s[6:7], 0, v[6:7]
	v_lshl_or_b32 v6, v6, 4, v76
	v_lshlrev_b32_e32 v155, 1, v6
	v_lshlrev_b64 v[6:7], 9, v[18:19]
	v_lshl_add_u64 v[56:57], v[2:3], 0, v[6:7]
	v_lshl_add_u64 v[6:7], v[18:19], 4, s[8:9]
	global_load_dword v82, v[6:7], off
	v_or_b32_e32 v6, 18, v0
	v_mov_b32_e32 v7, v1
	v_lshl_add_u64 v[16:17], s[6:7], 0, v[6:7]
	v_lshl_or_b32 v6, v6, 4, v76
	v_lshlrev_b32_e32 v158, 1, v6
	v_lshlrev_b64 v[6:7], 9, v[16:17]
	v_lshl_add_u64 v[58:59], v[2:3], 0, v[6:7]
	v_lshl_add_u64 v[6:7], v[16:17], 4, s[8:9]
	global_load_dword v81, v[6:7], off
	v_or_b32_e32 v6, 19, v68
	v_mov_b32_e32 v7, v1
	v_lshl_add_u64 v[14:15], s[6:7], 0, v[6:7]
	v_lshl_or_b32 v6, v6, 4, v76
	v_lshlrev_b32_e32 v160, 1, v6
	v_lshlrev_b64 v[6:7], 9, v[14:15]
	v_lshl_add_u64 v[60:61], v[2:3], 0, v[6:7]
	v_lshl_add_u64 v[6:7], v[14:15], 4, s[8:9]
	global_load_dword v80, v[6:7], off
	v_or_b32_e32 v6, 24, v0
	v_mov_b32_e32 v7, v1
	v_lshl_add_u64 v[12:13], s[6:7], 0, v[6:7]
	v_lshl_or_b32 v6, v6, 4, v76
	v_lshlrev_b32_e32 v162, 1, v6
	v_lshlrev_b64 v[6:7], 9, v[12:13]
	v_lshl_add_u64 v[62:63], v[2:3], 0, v[6:7]
	v_lshl_add_u64 v[6:7], v[12:13], 4, s[8:9]
	global_load_dword v79, v[6:7], off
	v_or_b32_e32 v6, 25, v0
	v_mov_b32_e32 v7, v1
	v_lshl_add_u64 v[10:11], s[6:7], 0, v[6:7]
	v_lshl_or_b32 v6, v6, 4, v76
	v_lshlrev_b32_e32 v164, 1, v6
	v_lshlrev_b64 v[6:7], 9, v[10:11]
	v_or_b32_e32 v0, 26, v0
	v_lshl_add_u64 v[64:65], v[2:3], 0, v[6:7]
	v_lshl_add_u64 v[6:7], v[10:11], 4, s[8:9]
	v_lshl_add_u64 v[8:9], s[6:7], 0, v[0:1]
	global_load_dword v78, v[6:7], off
	v_lshl_or_b32 v0, v0, 4, v76
	v_lshlrev_b64 v[6:7], 9, v[8:9]
	v_lshlrev_b32_e32 v166, 1, v0
	v_lshl_add_u64 v[66:67], v[2:3], 0, v[6:7]
	v_lshl_add_u64 v[6:7], v[8:9], 4, s[8:9]
	v_or_b32_e32 v0, 27, v68
	global_load_dword v77, v[6:7], off
	v_lshl_add_u64 v[6:7], s[6:7], 0, v[0:1]
	v_or_b32_e32 v83, 0x1000, v85
	v_lshl_or_b32 v0, v0, 4, v76
	v_lshl_add_u64 v[108:109], v[6:7], 4, s[8:9]
	v_lshlrev_b32_e32 v168, 1, v0
	global_load_dword v0, v[108:109], off
	global_load_ushort v105, v85, s[0:1]
	global_load_ushort v106, v83, s[0:1]
	v_mov_b32_e32 v109, v1
	global_load_ushort v85, v85, s[4:5]
	v_or_b32_e32 v87, 0x1000, v88
	global_load_ushort v83, v83, s[4:5]
	global_load_ushort v184, v[38:39], off
	global_load_ushort v185, v[38:39], off offset:64
	v_or_b32_e32 v89, 0x1000, v90
	v_or_b32_e32 v91, 0x1000, v92
	v_or_b32_e32 v94, 0x1000, v95
	v_or_b32_e32 v96, 0x1000, v97
	v_or_b32_e32 v98, 0x1000, v99
	v_or_b32_e32 v101, 0x1000, v102
	v_or_b32_e32 v103, 0x1000, v104
	v_lshlrev_b64 v[68:69], 9, v[6:7]
	v_lshlrev_b64 v[36:37], 11, v[36:37]
	v_or_b32_e32 v154, 0x1000, v155
	v_or_b32_e32 v159, 0x1000, v158
	v_or_b32_e32 v161, 0x1000, v160
; __device__ __forceinline__ float bf2f(bf16_t b) { return __uint_as_float(((unsigned)b) << 16); }
; __device__ __forceinline__ bf16_t f2bf(float f) { unsigned u = __float_as_uint(f); u += 0x7FFFu + ((u >> 16) & 1u); return (bf16_t)(u >> 16); }
; __device__ __forceinline__ float frsq(float x) { return __builtin_amdgcn_rsqf(x); }
; __device__ __forceinline__ void r4_zero_state(const Params& p, int l, unsigned char* ws, unsigned char* ob, int bh, int lane) {
;     ...
;         for (int r = 0; r < 16; ++r) { const int t = 32 * rb + (r & 3) + 8 * (r >> 2) + 4 * hi; const size_t row = (size_t)b * LT + t;
;             y0s[r] = YLg[TM(t, l31)]; y1s[r] = YLg[TM(t, 32 + l31)]; v0[r] = VVg[TM(t, l31)]; v1[r] = VVg[TM(t, 32 + l31)];
;             g0[r] = Gg[row * 256 + h * 64 + l31]; g1[r] = Gg[row * 256 + h * 64 + 32 + l31]; bcv[r] = BCg[row * 4 + h]; }
; #pragma unroll
;         for (int r = 0; r < 16; ++r) { const int t = 32 * rb + (r & 3) + 8 * (r >> 2) + 4 * hi; const size_t row = (size_t)b * LT + t;
;             const float y0 = bf2f(y0s[r]), y1 = bf2f(y1s[r]);
;             const float mean = half_sum32(y0 + y1) * (1.f / 64.f); const float d0 = y0 - mean, d1 = y1 - mean;
;             const float var = half_sum32(d0 * d0 + d1 * d1) * (1.f / 64.f); const float rs = frsq(var + 64e-5f);
;             const float o0 = (d0 * rs * lg0 + lb0 + bcv[r] * bf2f(v0[r])) * bf2f(g0[r]);
;             const float o1 = (d1 * rs * lg1 + lb1 + bcv[r] * bf2f(v1[r])) * bf2f(g1[r]);
;             MIX[row * D + M_C + h * 64 + l31] = f2bf(o0); MIX[row * D + M_C + h * 64 + 32 + l31] = f2bf(o1); }
	v_or_b32_e32 v163, 0x1000, v162
	v_or_b32_e32 v165, 0x1000, v164
	v_or_b32_e32 v167, 0x1000, v166
	v_or_b32_e32 v169, 0x1000, v168
	v_lshl_add_u64 v[68:69], v[2:3], 0, v[68:69]
	v_lshl_add_u64 v[156:157], v[4:5], 0, v[36:37]
	v_lshlrev_b64 v[34:35], 11, v[34:35]
	v_lshl_add_u64 v[34:35], v[4:5], 0, v[34:35]
	v_lshlrev_b64 v[32:33], 11, v[32:33]
	v_lshl_add_u64 v[32:33], v[4:5], 0, v[32:33]
	v_lshlrev_b64 v[30:31], 11, v[30:31]
	v_lshl_add_u64 v[30:31], v[4:5], 0, v[30:31]
	v_lshlrev_b64 v[28:29], 11, v[28:29]
	v_lshl_add_u64 v[28:29], v[4:5], 0, v[28:29]
	v_lshlrev_b64 v[26:27], 11, v[26:27]
	v_lshl_add_u64 v[26:27], v[4:5], 0, v[26:27]
	v_lshlrev_b64 v[24:25], 11, v[24:25]
	v_lshl_add_u64 v[24:25], v[4:5], 0, v[24:25]
	v_lshlrev_b64 v[22:23], 11, v[22:23]
	v_lshl_add_u64 v[22:23], v[4:5], 0, v[22:23]
	v_lshlrev_b64 v[20:21], 11, v[20:21]
	v_lshl_add_u64 v[20:21], v[4:5], 0, v[20:21]
	v_lshlrev_b64 v[18:19], 11, v[18:19]
	v_lshl_add_u64 v[18:19], v[4:5], 0, v[18:19]
	v_lshlrev_b64 v[16:17], 11, v[16:17]
	v_lshl_add_u64 v[16:17], v[4:5], 0, v[16:17]
	v_lshlrev_b64 v[14:15], 11, v[14:15]
	v_lshl_add_u64 v[14:15], v[4:5], 0, v[14:15]
	v_lshlrev_b64 v[12:13], 11, v[12:13]
	v_lshl_add_u64 v[12:13], v[4:5], 0, v[12:13]
	v_lshlrev_b64 v[10:11], 11, v[10:11]
	v_lshl_add_u64 v[10:11], v[4:5], 0, v[10:11]
	v_lshlrev_b64 v[8:9], 11, v[8:9]
	v_lshl_add_u64 v[8:9], v[4:5], 0, v[8:9]
	v_lshlrev_b64 v[6:7], 11, v[6:7]
	v_lshl_add_u64 v[6:7], v[4:5], 0, v[6:7]
	s_mov_b32 s16, 32
	s_and_b64 vcc, exec, vcc
	s_waitcnt vmcnt(3)
	v_lshlrev_b32_e32 v105, 16, v105
	s_waitcnt vmcnt(2)
	v_lshlrev_b32_e32 v106, 16, v106
	v_add_f32_e32 v108, v105, v106
	s_waitcnt vmcnt(1)
	v_lshlrev_b32_e32 v85, 16, v85
	s_waitcnt vmcnt(0)
	v_lshlrev_b32_e32 v83, 16, v83
	v_add_f32_dpp v108, v108, v108 quad_perm:[1,0,3,2] row_mask:0xf bank_mask:0xf bound_ctrl:1
	s_nop 1
	v_add_f32_dpp v108, v108, v108 quad_perm:[2,3,0,1] row_mask:0xf bank_mask:0xf bound_ctrl:1
	s_nop 1
	v_add_f32_dpp v108, v108, v108 row_half_mirror row_mask:0xf bank_mask:0xf bound_ctrl:1
	s_nop 1
	v_add_f32_dpp v108, v108, v108 row_mirror row_mask:0xf bank_mask:0xf bound_ctrl:1
	s_nop 1
	v_mov_b32_dpp v109, v108 row_bcast:15 row_mask:0xa bank_mask:0xf
	v_add_f32_e32 v108, v108, v109
	s_nop 0
	v_readlane_b32 s10, v108, 31
	v_readlane_b32 s11, v108, 63
	s_nop 0
	v_mov_b32_e32 v109, s10
	v_mov_b32_e32 v108, s11
	v_cndmask_b32_e64 v108, v108, v109, s[2:3]
	v_fmac_f32_e32 v106, 0xbc800000, v108
	v_fmac_f32_e32 v105, 0xbc800000, v108
	v_mul_f32_e32 v108, v106, v106
	v_fmac_f32_e32 v108, v105, v105
	v_mov_b32_e32 v109, v1
	s_nop 0
	v_add_f32_dpp v108, v108, v108 quad_perm:[1,0,3,2] row_mask:0xf bank_mask:0xf bound_ctrl:1
	s_nop 1
	v_add_f32_dpp v108, v108, v108 quad_perm:[2,3,0,1] row_mask:0xf bank_mask:0xf bound_ctrl:1
	s_nop 1
	v_add_f32_dpp v108, v108, v108 row_half_mirror row_mask:0xf bank_mask:0xf bound_ctrl:1
	s_nop 1
	v_add_f32_dpp v108, v108, v108 row_mirror row_mask:0xf bank_mask:0xf bound_ctrl:1
	s_nop 1
	v_mov_b32_dpp v109, v108 row_bcast:15 row_mask:0xa bank_mask:0xf
	v_add_f32_e32 v108, v108, v109
	s_nop 0
	v_readlane_b32 s10, v108, 31
	v_readlane_b32 s11, v108, 63
	s_nop 0
	v_mov_b32_e32 v109, s10
	v_mov_b32_e32 v108, s11
	v_cndmask_b32_e64 v108, v108, v109, s[2:3]
	v_fmamk_f32 v108, v108, 0x3c800000, v249
	v_rsq_f32_e32 v108, v108
	s_nop 0
	v_mul_f32_e32 v105, v105, v108
	v_fma_f32 v105, v70, v105, v72
	v_fmac_f32_e32 v105, v84, v85
	v_mov_b32_e32 v85, v184
	s_nop 0
	v_lshlrev_b32_e32 v85, 16, v85
	s_nop 0
	v_mul_f32_e32 v85, v105, v85
	v_mul_f32_e32 v105, v106, v108
	v_fma_f32 v105, v71, v105, v73
	v_fmac_f32_e32 v105, v84, v83
	v_mov_b32_e32 v38, v185
	v_lshlrev_b32_e32 v38, 16, v38
	v_mul_f32_e32 v170, v105, v38
	v_bfe_u32 v38, v85, 16, 1
	v_add3_u32 v171, v85, v38, s79
	global_load_ushort v172, v88, s[0:1]
	global_load_ushort v173, v87, s[0:1]
	global_load_ushort v153, v88, s[4:5]
	global_load_ushort v152, v[40:41], off
	global_load_ushort v151, v87, s[4:5]
	global_load_ushort v150, v[40:41], off offset:64
	global_load_ushort v148, v90, s[0:1]
	global_load_ushort v149, v89, s[0:1]
	global_load_ushort v147, v90, s[4:5]
	global_load_ushort v146, v[42:43], off
	global_load_ushort v145, v89, s[4:5]
	global_load_ushort v144, v[42:43], off offset:64
	global_load_ushort v142, v92, s[0:1]
	global_load_ushort v143, v91, s[0:1]
	global_load_ushort v141, v92, s[4:5]
	global_load_ushort v140, v[44:45], off
	global_load_ushort v139, v91, s[4:5]
	global_load_ushort v138, v[44:45], off offset:64
	global_load_ushort v136, v95, s[0:1]
	global_load_ushort v137, v94, s[0:1]
	global_load_ushort v135, v95, s[4:5]
	global_load_ushort v134, v[46:47], off
	global_load_ushort v133, v94, s[4:5]
	global_load_ushort v132, v[46:47], off offset:64
	global_load_ushort v130, v97, s[0:1]
	global_load_ushort v131, v96, s[0:1]
	global_load_ushort v128, v97, s[4:5]
	global_load_ushort v127, v[48:49], off
	global_load_ushort v126, v96, s[4:5]
	global_load_ushort v125, v[48:49], off offset:64
	global_load_ushort v123, v99, s[0:1]
	global_load_ushort v124, v98, s[0:1]
	global_load_ushort v121, v99, s[4:5]
	global_load_ushort v120, v[50:51], off
	global_load_ushort v119, v98, s[4:5]
	global_load_ushort v117, v[50:51], off offset:64
	global_load_ushort v115, v102, s[0:1]
	global_load_ushort v116, v101, s[0:1]
	global_load_ushort v113, v102, s[4:5]
	global_load_ushort v112, v[52:53], off
	global_load_ushort v111, v101, s[4:5]
	global_load_ushort v110, v[52:53], off offset:64
	global_load_ushort v108, v104, s[0:1]
	global_load_ushort v109, v103, s[0:1]
	global_load_ushort v106, v104, s[4:5]
	global_load_ushort v105, v[54:55], off
	s_nop 0
; __device__ __forceinline__ float bf2f(bf16_t b) { return __uint_as_float(((unsigned)b) << 16); }
; __device__ __forceinline__ bf16_t f2bf(float f) { unsigned u = __float_as_uint(f); u += 0x7FFFu + ((u >> 16) & 1u); return (bf16_t)(u >> 16); }
; __device__ __forceinline__ float frsq(float x) { return __builtin_amdgcn_rsqf(x); }
; __device__ __forceinline__ void r4_zero_state(const Params& p, int l, unsigned char* ws, unsigned char* ob, int bh, int lane) {
;     ...
;         for (int r = 0; r < 16; ++r) { const int t = 32 * rb + (r & 3) + 8 * (r >> 2) + 4 * hi; const size_t row = (size_t)b * LT + t;
;             y0s[r] = YLg[TM(t, l31)]; y1s[r] = YLg[TM(t, 32 + l31)]; v0[r] = VVg[TM(t, l31)]; v1[r] = VVg[TM(t, 32 + l31)];
;             g0[r] = Gg[row * 256 + h * 64 + l31]; g1[r] = Gg[row * 256 + h * 64 + 32 + l31]; bcv[r] = BCg[row * 4 + h]; }
; #pragma unroll
;         for (int r = 0; r < 16; ++r) { const int t = 32 * rb + (r & 3) + 8 * (r >> 2) + 4 * hi; const size_t row = (size_t)b * LT + t;
;             const float y0 = bf2f(y0s[r]), y1 = bf2f(y1s[r]);
;             const float mean = half_sum32(y0 + y1) * (1.f / 64.f); const float d0 = y0 - mean, d1 = y1 - mean;
;             const float var = half_sum32(d0 * d0 + d1 * d1) * (1.f / 64.f); const float rs = frsq(var + 64e-5f);
;             const float o0 = (d0 * rs * lg0 + lb0 + bcv[r] * bf2f(v0[r])) * bf2f(g0[r]);
;             const float o1 = (d1 * rs * lg1 + lb1 + bcv[r] * bf2f(v1[r])) * bf2f(g1[r]);
;             MIX[row * D + M_C + h * 64 + l31] = f2bf(o0); MIX[row * D + M_C + h * 64 + 32 + l31] = f2bf(o1); }
	global_load_ushort v104, v103, s[4:5]
	s_nop 0
	global_load_ushort v103, v[54:55], off offset:64
	global_load_ushort v101, v155, s[0:1]
	global_load_ushort v102, v154, s[0:1]
	global_load_ushort v99, v155, s[4:5]
	global_load_ushort v98, v[56:57], off
	global_load_ushort v97, v154, s[4:5]
	global_load_ushort v96, v[56:57], off offset:64
	global_load_ushort v94, v158, s[0:1]
	global_load_ushort v95, v159, s[0:1]
	global_load_ushort v92, v158, s[4:5]
	global_load_ushort v91, v[58:59], off
	global_load_ushort v90, v159, s[4:5]
	global_load_ushort v89, v[58:59], off offset:64
	global_load_ushort v87, v160, s[0:1]
	global_load_ushort v88, v161, s[0:1]
	global_load_ushort v85, v160, s[4:5]
	global_load_ushort v84, v[60:61], off
	global_load_ushort v83, v161, s[4:5]
	s_nop 0
	global_load_ushort v60, v[60:61], off offset:64
	s_nop 0
	global_load_ushort v58, v162, s[0:1]
	global_load_ushort v59, v163, s[0:1]
	global_load_ushort v57, v162, s[4:5]
	global_load_ushort v56, v[62:63], off
	global_load_ushort v55, v163, s[4:5]
	global_load_ushort v54, v[62:63], off offset:64
	global_load_ushort v52, v164, s[0:1]
	global_load_ushort v53, v165, s[0:1]
	global_load_ushort v51, v164, s[4:5]
	global_load_ushort v50, v[64:65], off
	global_load_ushort v49, v165, s[4:5]
	global_load_ushort v48, v[64:65], off offset:64
	global_load_ushort v46, v166, s[0:1]
	global_load_ushort v47, v167, s[0:1]
	global_load_ushort v45, v166, s[4:5]
	global_load_ushort v44, v[66:67], off
	global_load_ushort v43, v167, s[4:5]
	global_load_ushort v42, v[66:67], off offset:64
	global_load_ushort v40, v168, s[0:1]
	global_load_ushort v41, v169, s[0:1]
	global_load_ushort v39, v168, s[4:5]
	global_load_ushort v38, v[68:69], off
	global_load_ushort v37, v169, s[4:5]
	global_load_ushort v36, v[68:69], off offset:64
	v_bfe_u32 v61, v170, 16, 1
	v_add3_u32 v61, v170, v61, s79
	global_store_short_d16_hi v[156:157], v61, off offset:1088
	s_waitcnt vmcnt(62)
	v_lshlrev_b32_e32 v62, 16, v172
	v_lshlrev_b32_e32 v61, 16, v173
	v_add_f32_e32 v63, v62, v61
	v_mov_b32_e32 v64, v1
	global_store_short_d16_hi v[156:157], v171, off offset:1024
	v_add_f32_dpp v63, v63, v63 quad_perm:[1,0,3,2] row_mask:0xf bank_mask:0xf bound_ctrl:1
	s_nop 1
	v_add_f32_dpp v63, v63, v63 quad_perm:[2,3,0,1] row_mask:0xf bank_mask:0xf bound_ctrl:1
	s_nop 1
	v_add_f32_dpp v63, v63, v63 row_half_mirror row_mask:0xf bank_mask:0xf bound_ctrl:1
	s_nop 1
	v_add_f32_dpp v63, v63, v63 row_mirror row_mask:0xf bank_mask:0xf bound_ctrl:1
	s_nop 1
	v_mov_b32_dpp v64, v63 row_bcast:15 row_mask:0xa bank_mask:0xf
	v_add_f32_e32 v63, v63, v64
	s_nop 0
	v_readlane_b32 s10, v63, 31
	v_readlane_b32 s11, v63, 63
	s_nop 0
	v_mov_b32_e32 v64, s10
	v_mov_b32_e32 v63, s11
	v_cndmask_b32_e64 v63, v63, v64, s[2:3]
	v_fmac_f32_e32 v61, 0xbc800000, v63
	v_fmac_f32_e32 v62, 0xbc800000, v63
	v_mul_f32_e32 v63, v61, v61
	v_fmac_f32_e32 v63, v62, v62
	v_mov_b32_e32 v64, v1
	s_nop 0
	v_add_f32_dpp v63, v63, v63 quad_perm:[1,0,3,2] row_mask:0xf bank_mask:0xf bound_ctrl:1
	s_nop 1
	v_add_f32_dpp v63, v63, v63 quad_perm:[2,3,0,1] row_mask:0xf bank_mask:0xf bound_ctrl:1
	s_nop 1
	v_add_f32_dpp v63, v63, v63 row_half_mirror row_mask:0xf bank_mask:0xf bound_ctrl:1
	s_nop 1
	v_add_f32_dpp v63, v63, v63 row_mirror row_mask:0xf bank_mask:0xf bound_ctrl:1
	s_nop 1
	v_mov_b32_dpp v64, v63 row_bcast:15 row_mask:0xa bank_mask:0xf
	v_add_f32_e32 v63, v63, v64
	s_nop 0
	v_readlane_b32 s10, v63, 31
	v_readlane_b32 s11, v63, 63
	s_nop 0
	v_mov_b32_e32 v64, s10
	v_mov_b32_e32 v63, s11
	v_cndmask_b32_e64 v63, v63, v64, s[2:3]
	v_fmamk_f32 v63, v63, 0x3c800000, v249
	v_rsq_f32_e32 v63, v63
	v_lshlrev_b32_e32 v64, 16, v153
	v_mul_f32_e32 v62, v62, v63
	v_fma_f32 v62, v70, v62, v72
	v_mul_f32_e32 v61, v61, v63
	v_fmac_f32_e32 v62, v129, v64
	v_lshlrev_b32_e32 v64, 16, v152
	v_fma_f32 v61, v71, v61, v73
	v_lshlrev_b32_e32 v63, 16, v151
	v_mul_f32_e32 v62, v62, v64
	v_fmac_f32_e32 v61, v129, v63
	v_lshlrev_b32_e32 v63, 16, v150
	v_mul_f32_e32 v61, v61, v63
	v_bfe_u32 v63, v62, 16, 1
	v_add3_u32 v62, v62, v63, s79
	global_store_short_d16_hi v[34:35], v62, off offset:1024
	v_bfe_u32 v62, v61, 16, 1
	v_add3_u32 v61, v61, v62, s79
	global_store_short_d16_hi v[34:35], v61, off offset:1088
	v_lshlrev_b32_e32 v34, 16, v148
	v_lshlrev_b32_e32 v35, 16, v149
	v_add_f32_e32 v61, v34, v35
	v_mov_b32_e32 v62, v1
	s_nop 0
	v_add_f32_dpp v61, v61, v61 quad_perm:[1,0,3,2] row_mask:0xf bank_mask:0xf bound_ctrl:1
	s_nop 1
	v_add_f32_dpp v61, v61, v61 quad_perm:[2,3,0,1] row_mask:0xf bank_mask:0xf bound_ctrl:1
	s_nop 1
	v_add_f32_dpp v61, v61, v61 row_half_mirror row_mask:0xf bank_mask:0xf bound_ctrl:1
	s_nop 1
	v_add_f32_dpp v61, v61, v61 row_mirror row_mask:0xf bank_mask:0xf bound_ctrl:1
	s_nop 1
	v_mov_b32_dpp v62, v61 row_bcast:15 row_mask:0xa bank_mask:0xf
	v_add_f32_e32 v61, v61, v62
	s_nop 0
	v_readlane_b32 s10, v61, 31
	v_readlane_b32 s11, v61, 63
	s_nop 0
	v_mov_b32_e32 v62, s10
	v_mov_b32_e32 v61, s11
	v_cndmask_b32_e64 v61, v61, v62, s[2:3]
	v_fmac_f32_e32 v35, 0xbc800000, v61
	v_fmac_f32_e32 v34, 0xbc800000, v61
	v_mul_f32_e32 v61, v35, v35
	v_fmac_f32_e32 v61, v34, v34
	v_mov_b32_e32 v62, v1
	s_nop 0
	v_add_f32_dpp v61, v61, v61 quad_perm:[1,0,3,2] row_mask:0xf bank_mask:0xf bound_ctrl:1
	s_nop 1
	v_add_f32_dpp v61, v61, v61 quad_perm:[2,3,0,1] row_mask:0xf bank_mask:0xf bound_ctrl:1
	s_nop 1
	v_add_f32_dpp v61, v61, v61 row_half_mirror row_mask:0xf bank_mask:0xf bound_ctrl:1
	s_nop 1
	v_add_f32_dpp v61, v61, v61 row_mirror row_mask:0xf bank_mask:0xf bound_ctrl:1
	s_nop 1
	v_mov_b32_dpp v62, v61 row_bcast:15 row_mask:0xa bank_mask:0xf
	v_add_f32_e32 v61, v61, v62
	s_nop 0
; __device__ __forceinline__ float bf2f(bf16_t b) { return __uint_as_float(((unsigned)b) << 16); }
; __device__ __forceinline__ bf16_t f2bf(float f) { unsigned u = __float_as_uint(f); u += 0x7FFFu + ((u >> 16) & 1u); return (bf16_t)(u >> 16); }
; __device__ __forceinline__ float frsq(float x) { return __builtin_amdgcn_rsqf(x); }
; __device__ __forceinline__ void r4_zero_state(const Params& p, int l, unsigned char* ws, unsigned char* ob, int bh, int lane) {
;     ...
;         for (int r = 0; r < 16; ++r) { const int t = 32 * rb + (r & 3) + 8 * (r >> 2) + 4 * hi; const size_t row = (size_t)b * LT + t;
;             const float y0 = bf2f(y0s[r]), y1 = bf2f(y1s[r]);
;             const float mean = half_sum32(y0 + y1) * (1.f / 64.f); const float d0 = y0 - mean, d1 = y1 - mean;
;             const float var = half_sum32(d0 * d0 + d1 * d1) * (1.f / 64.f); const float rs = frsq(var + 64e-5f);
;             const float o0 = (d0 * rs * lg0 + lb0 + bcv[r] * bf2f(v0[r])) * bf2f(g0[r]);
;             const float o1 = (d1 * rs * lg1 + lb1 + bcv[r] * bf2f(v1[r])) * bf2f(g1[r]);
;             MIX[row * D + M_C + h * 64 + l31] = f2bf(o0); MIX[row * D + M_C + h * 64 + 32 + l31] = f2bf(o1); }
	v_readlane_b32 s10, v61, 31
	v_readlane_b32 s11, v61, 63
	s_nop 0
	v_mov_b32_e32 v62, s10
	v_mov_b32_e32 v61, s11
	v_cndmask_b32_e64 v61, v61, v62, s[2:3]
	v_fmamk_f32 v61, v61, 0x3c800000, v249
	v_rsq_f32_e32 v61, v61
	v_lshlrev_b32_e32 v62, 16, v147
	v_mul_f32_e32 v34, v34, v61
	v_fma_f32 v34, v70, v34, v72
	v_mul_f32_e32 v35, v35, v61
	v_fmac_f32_e32 v34, v122, v62
	v_lshlrev_b32_e32 v62, 16, v146
	v_fma_f32 v35, v71, v35, v73
	v_lshlrev_b32_e32 v61, 16, v145
	v_mul_f32_e32 v34, v34, v62
	v_fmac_f32_e32 v35, v122, v61
	v_lshlrev_b32_e32 v61, 16, v144
	v_mul_f32_e32 v35, v35, v61
	v_bfe_u32 v61, v34, 16, 1
	v_add3_u32 v34, v34, v61, s79
	global_store_short_d16_hi v[32:33], v34, off offset:1024
	v_bfe_u32 v34, v35, 16, 1
	v_add3_u32 v34, v35, v34, s79
	global_store_short_d16_hi v[32:33], v34, off offset:1088
	v_lshlrev_b32_e32 v32, 16, v142
	v_lshlrev_b32_e32 v33, 16, v143
	v_add_f32_e32 v34, v32, v33
	v_mov_b32_e32 v35, v1
	s_nop 0
	v_add_f32_dpp v34, v34, v34 quad_perm:[1,0,3,2] row_mask:0xf bank_mask:0xf bound_ctrl:1
	s_nop 1
	v_add_f32_dpp v34, v34, v34 quad_perm:[2,3,0,1] row_mask:0xf bank_mask:0xf bound_ctrl:1
	s_nop 1
	v_add_f32_dpp v34, v34, v34 row_half_mirror row_mask:0xf bank_mask:0xf bound_ctrl:1
	s_nop 1
	v_add_f32_dpp v34, v34, v34 row_mirror row_mask:0xf bank_mask:0xf bound_ctrl:1
	s_nop 1
	v_mov_b32_dpp v35, v34 row_bcast:15 row_mask:0xa bank_mask:0xf
	v_add_f32_e32 v34, v34, v35
	s_nop 0
	v_readlane_b32 s10, v34, 31
	v_readlane_b32 s11, v34, 63
	s_nop 0
	v_mov_b32_e32 v35, s10
	v_mov_b32_e32 v34, s11
	v_cndmask_b32_e64 v34, v34, v35, s[2:3]
	v_fmac_f32_e32 v33, 0xbc800000, v34
	v_fmac_f32_e32 v32, 0xbc800000, v34
	v_mul_f32_e32 v34, v33, v33
	v_fmac_f32_e32 v34, v32, v32
	v_mov_b32_e32 v35, v1
	s_nop 0
	v_add_f32_dpp v34, v34, v34 quad_perm:[1,0,3,2] row_mask:0xf bank_mask:0xf bound_ctrl:1
	s_nop 1
	v_add_f32_dpp v34, v34, v34 quad_perm:[2,3,0,1] row_mask:0xf bank_mask:0xf bound_ctrl:1
	s_nop 1
	v_add_f32_dpp v34, v34, v34 row_half_mirror row_mask:0xf bank_mask:0xf bound_ctrl:1
	s_nop 1
	v_add_f32_dpp v34, v34, v34 row_mirror row_mask:0xf bank_mask:0xf bound_ctrl:1
	s_nop 1
	v_mov_b32_dpp v35, v34 row_bcast:15 row_mask:0xa bank_mask:0xf
	v_add_f32_e32 v34, v34, v35
	s_nop 0
	v_readlane_b32 s10, v34, 31
	v_readlane_b32 s11, v34, 63
	s_nop 0
	v_mov_b32_e32 v35, s10
	v_mov_b32_e32 v34, s11
	v_cndmask_b32_e64 v34, v34, v35, s[2:3]
	v_fmamk_f32 v34, v34, 0x3c800000, v249
	v_rsq_f32_e32 v34, v34
	v_lshlrev_b32_e32 v35, 16, v141
	v_mul_f32_e32 v32, v32, v34
	v_fma_f32 v32, v70, v32, v72
	v_mul_f32_e32 v33, v33, v34
	v_fmac_f32_e32 v32, v118, v35
	v_lshlrev_b32_e32 v35, 16, v140
	v_fma_f32 v33, v71, v33, v73
	v_lshlrev_b32_e32 v34, 16, v139
	v_mul_f32_e32 v32, v32, v35
	v_fmac_f32_e32 v33, v118, v34
	v_lshlrev_b32_e32 v34, 16, v138
	v_mul_f32_e32 v33, v33, v34
	v_bfe_u32 v34, v32, 16, 1
	v_add3_u32 v32, v32, v34, s79
	global_store_short_d16_hi v[30:31], v32, off offset:1024
	v_bfe_u32 v32, v33, 16, 1
	v_add3_u32 v32, v33, v32, s79
	global_store_short_d16_hi v[30:31], v32, off offset:1088
	v_lshlrev_b32_e32 v30, 16, v136
	v_lshlrev_b32_e32 v31, 16, v137
	v_add_f32_e32 v32, v30, v31
	v_mov_b32_e32 v33, v1
	s_nop 0
	v_add_f32_dpp v32, v32, v32 quad_perm:[1,0,3,2] row_mask:0xf bank_mask:0xf bound_ctrl:1
	s_nop 1
	v_add_f32_dpp v32, v32, v32 quad_perm:[2,3,0,1] row_mask:0xf bank_mask:0xf bound_ctrl:1
	s_nop 1
	v_add_f32_dpp v32, v32, v32 row_half_mirror row_mask:0xf bank_mask:0xf bound_ctrl:1
	s_nop 1
	v_add_f32_dpp v32, v32, v32 row_mirror row_mask:0xf bank_mask:0xf bound_ctrl:1
	s_nop 1
	v_mov_b32_dpp v33, v32 row_bcast:15 row_mask:0xa bank_mask:0xf
	v_add_f32_e32 v32, v32, v33
	s_nop 0
	v_readlane_b32 s10, v32, 31
	v_readlane_b32 s11, v32, 63
	s_nop 0
	v_mov_b32_e32 v33, s10
	v_mov_b32_e32 v32, s11
	v_cndmask_b32_e64 v32, v32, v33, s[2:3]
	v_fmac_f32_e32 v31, 0xbc800000, v32
	v_fmac_f32_e32 v30, 0xbc800000, v32
	v_mul_f32_e32 v32, v31, v31
	v_fmac_f32_e32 v32, v30, v30
	v_mov_b32_e32 v33, v1
	s_nop 0
	v_add_f32_dpp v32, v32, v32 quad_perm:[1,0,3,2] row_mask:0xf bank_mask:0xf bound_ctrl:1
	s_nop 1
	v_add_f32_dpp v32, v32, v32 quad_perm:[2,3,0,1] row_mask:0xf bank_mask:0xf bound_ctrl:1
	s_nop 1
	v_add_f32_dpp v32, v32, v32 row_half_mirror row_mask:0xf bank_mask:0xf bound_ctrl:1
	s_nop 1
	v_add_f32_dpp v32, v32, v32 row_mirror row_mask:0xf bank_mask:0xf bound_ctrl:1
	s_nop 1
	v_mov_b32_dpp v33, v32 row_bcast:15 row_mask:0xa bank_mask:0xf
	v_add_f32_e32 v32, v32, v33
	s_nop 0
	v_readlane_b32 s10, v32, 31
	v_readlane_b32 s11, v32, 63
	s_nop 0
	v_mov_b32_e32 v33, s10
	v_mov_b32_e32 v32, s11
	v_cndmask_b32_e64 v32, v32, v33, s[2:3]
	v_fmamk_f32 v32, v32, 0x3c800000, v249
	v_rsq_f32_e32 v32, v32
	v_lshlrev_b32_e32 v33, 16, v135
	v_mul_f32_e32 v30, v30, v32
	v_fma_f32 v30, v70, v30, v72
	v_mul_f32_e32 v31, v31, v32
	v_fmac_f32_e32 v30, v114, v33
	v_lshlrev_b32_e32 v33, 16, v134
	v_fma_f32 v31, v71, v31, v73
	v_lshlrev_b32_e32 v32, 16, v133
	v_mul_f32_e32 v30, v30, v33
	v_fmac_f32_e32 v31, v114, v32
	v_lshlrev_b32_e32 v32, 16, v132
	v_mul_f32_e32 v31, v31, v32
	v_bfe_u32 v32, v30, 16, 1
	v_add3_u32 v30, v30, v32, s79
	global_store_short_d16_hi v[28:29], v30, off offset:1024
	v_bfe_u32 v30, v31, 16, 1
	v_add3_u32 v30, v31, v30, s79
	global_store_short_d16_hi v[28:29], v30, off offset:1088
	v_lshlrev_b32_e32 v28, 16, v130
	v_lshlrev_b32_e32 v29, 16, v131
	v_add_f32_e32 v30, v28, v29
	v_mov_b32_e32 v31, v1
	s_nop 0
	v_add_f32_dpp v30, v30, v30 quad_perm:[1,0,3,2] row_mask:0xf bank_mask:0xf bound_ctrl:1
	s_nop 1
	v_add_f32_dpp v30, v30, v30 quad_perm:[2,3,0,1] row_mask:0xf bank_mask:0xf bound_ctrl:1
	s_nop 1
; __device__ __forceinline__ float bf2f(bf16_t b) { return __uint_as_float(((unsigned)b) << 16); }
; __device__ __forceinline__ bf16_t f2bf(float f) { unsigned u = __float_as_uint(f); u += 0x7FFFu + ((u >> 16) & 1u); return (bf16_t)(u >> 16); }
; __device__ __forceinline__ float frsq(float x) { return __builtin_amdgcn_rsqf(x); }
; __device__ __forceinline__ void r4_zero_state(const Params& p, int l, unsigned char* ws, unsigned char* ob, int bh, int lane) {
;     ...
;         for (int r = 0; r < 16; ++r) { const int t = 32 * rb + (r & 3) + 8 * (r >> 2) + 4 * hi; const size_t row = (size_t)b * LT + t;
;             const float y0 = bf2f(y0s[r]), y1 = bf2f(y1s[r]);
;             const float mean = half_sum32(y0 + y1) * (1.f / 64.f); const float d0 = y0 - mean, d1 = y1 - mean;
;             const float var = half_sum32(d0 * d0 + d1 * d1) * (1.f / 64.f); const float rs = frsq(var + 64e-5f);
;             const float o0 = (d0 * rs * lg0 + lb0 + bcv[r] * bf2f(v0[r])) * bf2f(g0[r]);
;             const float o1 = (d1 * rs * lg1 + lb1 + bcv[r] * bf2f(v1[r])) * bf2f(g1[r]);
;             MIX[row * D + M_C + h * 64 + l31] = f2bf(o0); MIX[row * D + M_C + h * 64 + 32 + l31] = f2bf(o1); }
	v_add_f32_dpp v30, v30, v30 row_half_mirror row_mask:0xf bank_mask:0xf bound_ctrl:1
	s_nop 1
	v_add_f32_dpp v30, v30, v30 row_mirror row_mask:0xf bank_mask:0xf bound_ctrl:1
	s_nop 1
	v_mov_b32_dpp v31, v30 row_bcast:15 row_mask:0xa bank_mask:0xf
	v_add_f32_e32 v30, v30, v31
	s_nop 0
	v_readlane_b32 s10, v30, 31
	v_readlane_b32 s11, v30, 63
	s_nop 0
	v_mov_b32_e32 v31, s10
	v_mov_b32_e32 v30, s11
	v_cndmask_b32_e64 v30, v30, v31, s[2:3]
	v_fmac_f32_e32 v29, 0xbc800000, v30
	v_fmac_f32_e32 v28, 0xbc800000, v30
	v_mul_f32_e32 v30, v29, v29
	v_fmac_f32_e32 v30, v28, v28
	v_mov_b32_e32 v31, v1
	s_nop 0
	v_add_f32_dpp v30, v30, v30 quad_perm:[1,0,3,2] row_mask:0xf bank_mask:0xf bound_ctrl:1
	s_nop 1
	v_add_f32_dpp v30, v30, v30 quad_perm:[2,3,0,1] row_mask:0xf bank_mask:0xf bound_ctrl:1
	s_nop 1
	v_add_f32_dpp v30, v30, v30 row_half_mirror row_mask:0xf bank_mask:0xf bound_ctrl:1
	s_nop 1
	v_add_f32_dpp v30, v30, v30 row_mirror row_mask:0xf bank_mask:0xf bound_ctrl:1
	s_nop 1
	v_mov_b32_dpp v31, v30 row_bcast:15 row_mask:0xa bank_mask:0xf
	v_add_f32_e32 v30, v30, v31
	s_nop 0
	v_readlane_b32 s10, v30, 31
	v_readlane_b32 s11, v30, 63
	s_nop 0
	v_mov_b32_e32 v31, s10
	v_mov_b32_e32 v30, s11
	v_cndmask_b32_e64 v30, v30, v31, s[2:3]
	v_fmamk_f32 v30, v30, 0x3c800000, v249
	v_rsq_f32_e32 v30, v30
	v_lshlrev_b32_e32 v31, 16, v128
	v_mul_f32_e32 v28, v28, v30
	v_fma_f32 v28, v70, v28, v72
	v_mul_f32_e32 v29, v29, v30
	v_fmac_f32_e32 v28, v107, v31
	v_lshlrev_b32_e32 v31, 16, v127
	v_fma_f32 v29, v71, v29, v73
	v_lshlrev_b32_e32 v30, 16, v126
	v_mul_f32_e32 v28, v28, v31
	v_fmac_f32_e32 v29, v107, v30
	s_waitcnt vmcnt(62)
	v_lshlrev_b32_e32 v30, 16, v125
	v_mul_f32_e32 v29, v29, v30
	v_bfe_u32 v30, v28, 16, 1
	v_add3_u32 v28, v28, v30, s79
	global_store_short_d16_hi v[26:27], v28, off offset:1024
	v_bfe_u32 v28, v29, 16, 1
	v_add3_u32 v28, v29, v28, s79
	global_store_short_d16_hi v[26:27], v28, off offset:1088
	v_lshlrev_b32_e32 v26, 16, v123
	v_lshlrev_b32_e32 v27, 16, v124
	v_add_f32_e32 v28, v26, v27
	v_mov_b32_e32 v29, v1
	s_nop 0
	v_add_f32_dpp v28, v28, v28 quad_perm:[1,0,3,2] row_mask:0xf bank_mask:0xf bound_ctrl:1
	s_nop 1
	v_add_f32_dpp v28, v28, v28 quad_perm:[2,3,0,1] row_mask:0xf bank_mask:0xf bound_ctrl:1
	s_nop 1
	v_add_f32_dpp v28, v28, v28 row_half_mirror row_mask:0xf bank_mask:0xf bound_ctrl:1
	s_nop 1
	v_add_f32_dpp v28, v28, v28 row_mirror row_mask:0xf bank_mask:0xf bound_ctrl:1
	s_nop 1
	v_mov_b32_dpp v29, v28 row_bcast:15 row_mask:0xa bank_mask:0xf
	v_add_f32_e32 v28, v28, v29
	s_nop 0
	v_readlane_b32 s10, v28, 31
	v_readlane_b32 s11, v28, 63
	s_nop 0
	v_mov_b32_e32 v29, s10
	v_mov_b32_e32 v28, s11
	v_cndmask_b32_e64 v28, v28, v29, s[2:3]
	v_fmac_f32_e32 v27, 0xbc800000, v28
	v_fmac_f32_e32 v26, 0xbc800000, v28
	v_mul_f32_e32 v28, v27, v27
	v_fmac_f32_e32 v28, v26, v26
	v_mov_b32_e32 v29, v1
	s_nop 0
	v_add_f32_dpp v28, v28, v28 quad_perm:[1,0,3,2] row_mask:0xf bank_mask:0xf bound_ctrl:1
	s_nop 1
	v_add_f32_dpp v28, v28, v28 quad_perm:[2,3,0,1] row_mask:0xf bank_mask:0xf bound_ctrl:1
	s_nop 1
	v_add_f32_dpp v28, v28, v28 row_half_mirror row_mask:0xf bank_mask:0xf bound_ctrl:1
	s_nop 1
	v_add_f32_dpp v28, v28, v28 row_mirror row_mask:0xf bank_mask:0xf bound_ctrl:1
	s_nop 1
	v_mov_b32_dpp v29, v28 row_bcast:15 row_mask:0xa bank_mask:0xf
	v_add_f32_e32 v28, v28, v29
	s_nop 0
	v_readlane_b32 s10, v28, 31
	v_readlane_b32 s11, v28, 63
	s_nop 0
	v_mov_b32_e32 v29, s10
	v_mov_b32_e32 v28, s11
	v_cndmask_b32_e64 v28, v28, v29, s[2:3]
	v_fmamk_f32 v28, v28, 0x3c800000, v249
	v_rsq_f32_e32 v28, v28
	v_lshlrev_b32_e32 v29, 16, v121
	v_mul_f32_e32 v26, v26, v28
	v_fma_f32 v26, v70, v26, v72
	v_mul_f32_e32 v27, v27, v28
	v_fmac_f32_e32 v26, v100, v29
	v_lshlrev_b32_e32 v29, 16, v120
	v_fma_f32 v27, v71, v27, v73
	v_lshlrev_b32_e32 v28, 16, v119
	v_mul_f32_e32 v26, v26, v29
	v_fmac_f32_e32 v27, v100, v28
	v_lshlrev_b32_e32 v28, 16, v117
	v_mul_f32_e32 v27, v27, v28
	v_bfe_u32 v28, v26, 16, 1
	v_add3_u32 v26, v26, v28, s79
	global_store_short_d16_hi v[24:25], v26, off offset:1024
	v_bfe_u32 v26, v27, 16, 1
	v_add3_u32 v26, v27, v26, s79
	global_store_short_d16_hi v[24:25], v26, off offset:1088
	v_lshlrev_b32_e32 v24, 16, v115
	v_lshlrev_b32_e32 v25, 16, v116
	v_add_f32_e32 v26, v24, v25
	v_mov_b32_e32 v27, v1
	s_nop 0
	v_add_f32_dpp v26, v26, v26 quad_perm:[1,0,3,2] row_mask:0xf bank_mask:0xf bound_ctrl:1
	s_nop 1
	v_add_f32_dpp v26, v26, v26 quad_perm:[2,3,0,1] row_mask:0xf bank_mask:0xf bound_ctrl:1
	s_nop 1
	v_add_f32_dpp v26, v26, v26 row_half_mirror row_mask:0xf bank_mask:0xf bound_ctrl:1
	s_nop 1
	v_add_f32_dpp v26, v26, v26 row_mirror row_mask:0xf bank_mask:0xf bound_ctrl:1
	s_nop 1
	v_mov_b32_dpp v27, v26 row_bcast:15 row_mask:0xa bank_mask:0xf
	v_add_f32_e32 v26, v26, v27
	s_nop 0
	v_readlane_b32 s10, v26, 31
	v_readlane_b32 s11, v26, 63
	s_nop 0
	v_mov_b32_e32 v27, s10
	v_mov_b32_e32 v26, s11
	v_cndmask_b32_e64 v26, v26, v27, s[2:3]
	v_fmac_f32_e32 v25, 0xbc800000, v26
	v_fmac_f32_e32 v24, 0xbc800000, v26
	v_mul_f32_e32 v26, v25, v25
	v_fmac_f32_e32 v26, v24, v24
	v_mov_b32_e32 v27, v1
	s_nop 0
	v_add_f32_dpp v26, v26, v26 quad_perm:[1,0,3,2] row_mask:0xf bank_mask:0xf bound_ctrl:1
	s_nop 1
	v_add_f32_dpp v26, v26, v26 quad_perm:[2,3,0,1] row_mask:0xf bank_mask:0xf bound_ctrl:1
	s_nop 1
	v_add_f32_dpp v26, v26, v26 row_half_mirror row_mask:0xf bank_mask:0xf bound_ctrl:1
	s_nop 1
	v_add_f32_dpp v26, v26, v26 row_mirror row_mask:0xf bank_mask:0xf bound_ctrl:1
	s_nop 1
	v_mov_b32_dpp v27, v26 row_bcast:15 row_mask:0xa bank_mask:0xf
	v_add_f32_e32 v26, v26, v27
	s_nop 0
	v_readlane_b32 s10, v26, 31
	v_readlane_b32 s11, v26, 63
	s_nop 0
	v_mov_b32_e32 v27, s10
	v_mov_b32_e32 v26, s11
	v_cndmask_b32_e64 v26, v26, v27, s[2:3]
	v_fmamk_f32 v26, v26, 0x3c800000, v249
	v_rsq_f32_e32 v26, v26
	s_waitcnt vmcnt(62)
; __device__ __forceinline__ float bf2f(bf16_t b) { return __uint_as_float(((unsigned)b) << 16); }
; __device__ __forceinline__ bf16_t f2bf(float f) { unsigned u = __float_as_uint(f); u += 0x7FFFu + ((u >> 16) & 1u); return (bf16_t)(u >> 16); }
; __device__ __forceinline__ float frsq(float x) { return __builtin_amdgcn_rsqf(x); }
; __device__ __forceinline__ float row_sum16(float v) {
;     v = dpp_add<0xB1, 0xF>(v); v = dpp_add<0x4E, 0xF>(v); v = dpp_add<0x141, 0xF>(v); v = dpp_add<0x140, 0xF>(v); return v;
; }
; __device__ __forceinline__ float wave_sum(float v) {
;     v = row_sum16(v); v = dpp_add<0x142, 0xA>(v); v = dpp_add<0x143, 0xC>(v);
;     return __int_as_float(__builtin_amdgcn_readlane(__float_as_int(v), 63));
; }
; __device__ __forceinline__ float half_sum32(float v) {
;     v = row_sum16(v); v = dpp_add<0x142, 0xA>(v);
;     const float lo = __int_as_float(__builtin_amdgcn_readlane(__float_as_int(v), 31)), hi = __int_as_float(__builtin_amdgcn_readlane(__float_as_int(v), 63));
;     return (__builtin_amdgcn_mbcnt_hi(~0u, __builtin_amdgcn_mbcnt_lo(~0u, 0u)) < 32u) ? lo : hi;
; }
; __device__ __forceinline__ void r4_zero_state(const Params& p, int l, unsigned char* ws, unsigned char* ob, int bh, int lane) {
;     ...
;         for (int r = 0; r < 16; ++r) { const int t = 32 * rb + (r & 3) + 8 * (r >> 2) + 4 * hi; const size_t row = (size_t)b * LT + t;
;             const float y0 = bf2f(y0s[r]), y1 = bf2f(y1s[r]);
;             const float mean = half_sum32(y0 + y1) * (1.f / 64.f); const float d0 = y0 - mean, d1 = y1 - mean;
;             const float var = half_sum32(d0 * d0 + d1 * d1) * (1.f / 64.f); const float rs = frsq(var + 64e-5f);
;             const float o0 = (d0 * rs * lg0 + lb0 + bcv[r] * bf2f(v0[r])) * bf2f(g0[r]);
;             const float o1 = (d1 * rs * lg1 + lb1 + bcv[r] * bf2f(v1[r])) * bf2f(g1[r]);
;             MIX[row * D + M_C + h * 64 + l31] = f2bf(o0); MIX[row * D + M_C + h * 64 + 32 + l31] = f2bf(o1); }
	v_lshlrev_b32_e32 v27, 16, v113
	v_mul_f32_e32 v24, v24, v26
	v_fma_f32 v24, v70, v24, v72
	v_mul_f32_e32 v25, v25, v26
	v_fmac_f32_e32 v24, v93, v27
	v_lshlrev_b32_e32 v27, 16, v112
	v_fma_f32 v25, v71, v25, v73
	v_lshlrev_b32_e32 v26, 16, v111
	v_mul_f32_e32 v24, v24, v27
	v_fmac_f32_e32 v25, v93, v26
	v_lshlrev_b32_e32 v26, 16, v110
	v_mul_f32_e32 v25, v25, v26
	v_bfe_u32 v26, v24, 16, 1
	v_add3_u32 v24, v24, v26, s79
	global_store_short_d16_hi v[22:23], v24, off offset:1024
	v_bfe_u32 v24, v25, 16, 1
	v_add3_u32 v24, v25, v24, s79
	global_store_short_d16_hi v[22:23], v24, off offset:1088
	s_waitcnt vmcnt(62)
	v_lshlrev_b32_e32 v22, 16, v108
	v_lshlrev_b32_e32 v23, 16, v109
	v_add_f32_e32 v24, v22, v23
	v_mov_b32_e32 v25, v1
	s_nop 0
	v_add_f32_dpp v24, v24, v24 quad_perm:[1,0,3,2] row_mask:0xf bank_mask:0xf bound_ctrl:1
	s_nop 1
	v_add_f32_dpp v24, v24, v24 quad_perm:[2,3,0,1] row_mask:0xf bank_mask:0xf bound_ctrl:1
	s_nop 1
	v_add_f32_dpp v24, v24, v24 row_half_mirror row_mask:0xf bank_mask:0xf bound_ctrl:1
	s_nop 1
	v_add_f32_dpp v24, v24, v24 row_mirror row_mask:0xf bank_mask:0xf bound_ctrl:1
	s_nop 1
	v_mov_b32_dpp v25, v24 row_bcast:15 row_mask:0xa bank_mask:0xf
	v_add_f32_e32 v24, v24, v25
	s_nop 0
	v_readlane_b32 s10, v24, 31
	v_readlane_b32 s11, v24, 63
	s_nop 0
	v_mov_b32_e32 v25, s10
	v_mov_b32_e32 v24, s11
	v_cndmask_b32_e64 v24, v24, v25, s[2:3]
	v_fmac_f32_e32 v23, 0xbc800000, v24
	v_fmac_f32_e32 v22, 0xbc800000, v24
	v_mul_f32_e32 v24, v23, v23
	v_fmac_f32_e32 v24, v22, v22
	v_mov_b32_e32 v25, v1
	s_nop 0
	v_add_f32_dpp v24, v24, v24 quad_perm:[1,0,3,2] row_mask:0xf bank_mask:0xf bound_ctrl:1
	s_nop 1
	v_add_f32_dpp v24, v24, v24 quad_perm:[2,3,0,1] row_mask:0xf bank_mask:0xf bound_ctrl:1
	s_nop 1
	v_add_f32_dpp v24, v24, v24 row_half_mirror row_mask:0xf bank_mask:0xf bound_ctrl:1
	s_nop 1
	v_add_f32_dpp v24, v24, v24 row_mirror row_mask:0xf bank_mask:0xf bound_ctrl:1
	s_nop 1
	v_mov_b32_dpp v25, v24 row_bcast:15 row_mask:0xa bank_mask:0xf
	v_add_f32_e32 v24, v24, v25
	s_nop 0
	v_readlane_b32 s10, v24, 31
	v_readlane_b32 s11, v24, 63
	s_nop 0
	v_mov_b32_e32 v25, s10
	v_mov_b32_e32 v24, s11
	v_cndmask_b32_e64 v24, v24, v25, s[2:3]
	v_fmamk_f32 v24, v24, 0x3c800000, v249
	v_rsq_f32_e32 v24, v24
	s_waitcnt vmcnt(61)
	v_lshlrev_b32_e32 v25, 16, v106
	v_mul_f32_e32 v22, v22, v24
	v_fma_f32 v22, v70, v22, v72
	v_mul_f32_e32 v23, v23, v24
	v_fmac_f32_e32 v22, v86, v25
	s_waitcnt vmcnt(60)
	v_lshlrev_b32_e32 v25, 16, v105
	v_fma_f32 v23, v71, v23, v73
	s_waitcnt vmcnt(59)
	v_lshlrev_b32_e32 v24, 16, v104
	v_mul_f32_e32 v22, v22, v25
	v_fmac_f32_e32 v23, v86, v24
	s_waitcnt vmcnt(58)
	v_lshlrev_b32_e32 v24, 16, v103
	v_mul_f32_e32 v23, v23, v24
	v_bfe_u32 v24, v22, 16, 1
	v_add3_u32 v22, v22, v24, s79
	global_store_short_d16_hi v[20:21], v22, off offset:1024
	v_bfe_u32 v22, v23, 16, 1
	v_add3_u32 v22, v23, v22, s79
	global_store_short_d16_hi v[20:21], v22, off offset:1088
	s_waitcnt vmcnt(59)
	v_lshlrev_b32_e32 v20, 16, v101
	s_waitcnt vmcnt(58)
	v_lshlrev_b32_e32 v21, 16, v102
	v_add_f32_e32 v22, v20, v21
	v_mov_b32_e32 v23, v1
	s_nop 0
	v_add_f32_dpp v22, v22, v22 quad_perm:[1,0,3,2] row_mask:0xf bank_mask:0xf bound_ctrl:1
	s_nop 1
	v_add_f32_dpp v22, v22, v22 quad_perm:[2,3,0,1] row_mask:0xf bank_mask:0xf bound_ctrl:1
	s_nop 1
	v_add_f32_dpp v22, v22, v22 row_half_mirror row_mask:0xf bank_mask:0xf bound_ctrl:1
	s_nop 1
	v_add_f32_dpp v22, v22, v22 row_mirror row_mask:0xf bank_mask:0xf bound_ctrl:1
	s_nop 1
	v_mov_b32_dpp v23, v22 row_bcast:15 row_mask:0xa bank_mask:0xf
	v_add_f32_e32 v22, v22, v23
	s_nop 0
	v_readlane_b32 s10, v22, 31
	v_readlane_b32 s11, v22, 63
	s_nop 0
	v_mov_b32_e32 v23, s10
	v_mov_b32_e32 v22, s11
	v_cndmask_b32_e64 v22, v22, v23, s[2:3]
	v_fmac_f32_e32 v21, 0xbc800000, v22
	v_fmac_f32_e32 v20, 0xbc800000, v22
	v_mul_f32_e32 v22, v21, v21
	v_fmac_f32_e32 v22, v20, v20
	v_mov_b32_e32 v23, v1
	s_nop 0
	v_add_f32_dpp v22, v22, v22 quad_perm:[1,0,3,2] row_mask:0xf bank_mask:0xf bound_ctrl:1
	s_nop 1
	v_add_f32_dpp v22, v22, v22 quad_perm:[2,3,0,1] row_mask:0xf bank_mask:0xf bound_ctrl:1
	s_nop 1
	v_add_f32_dpp v22, v22, v22 row_half_mirror row_mask:0xf bank_mask:0xf bound_ctrl:1
	s_nop 1
	v_add_f32_dpp v22, v22, v22 row_mirror row_mask:0xf bank_mask:0xf bound_ctrl:1
	s_nop 1
	v_mov_b32_dpp v23, v22 row_bcast:15 row_mask:0xa bank_mask:0xf
	v_add_f32_e32 v22, v22, v23
	s_nop 0
	v_readlane_b32 s10, v22, 31
	v_readlane_b32 s11, v22, 63
	s_nop 0
	v_mov_b32_e32 v23, s10
	v_mov_b32_e32 v22, s11
	v_cndmask_b32_e64 v22, v22, v23, s[2:3]
	v_fmamk_f32 v22, v22, 0x3c800000, v249
	v_rsq_f32_e32 v22, v22
	s_waitcnt vmcnt(57)
	v_lshlrev_b32_e32 v23, 16, v99
	v_mul_f32_e32 v20, v20, v22
	v_fma_f32 v20, v70, v20, v72
	v_mul_f32_e32 v21, v21, v22
	v_fmac_f32_e32 v20, v82, v23
	s_waitcnt vmcnt(56)
	v_lshlrev_b32_e32 v23, 16, v98
	v_fma_f32 v21, v71, v21, v73
	s_waitcnt vmcnt(55)
	v_lshlrev_b32_e32 v22, 16, v97
	v_mul_f32_e32 v20, v20, v23
	v_fmac_f32_e32 v21, v82, v22
	s_waitcnt vmcnt(54)
	v_lshlrev_b32_e32 v22, 16, v96
	v_mul_f32_e32 v21, v21, v22
	v_bfe_u32 v22, v20, 16, 1
	v_add3_u32 v20, v20, v22, s79
	global_store_short_d16_hi v[18:19], v20, off offset:1024
	v_bfe_u32 v20, v21, 16, 1
	v_add3_u32 v20, v21, v20, s79
	global_store_short_d16_hi v[18:19], v20, off offset:1088
	s_waitcnt vmcnt(55)
	v_lshlrev_b32_e32 v18, 16, v94
	s_waitcnt vmcnt(54)
; __device__ __forceinline__ float bf2f(bf16_t b) { return __uint_as_float(((unsigned)b) << 16); }
; __device__ __forceinline__ bf16_t f2bf(float f) { unsigned u = __float_as_uint(f); u += 0x7FFFu + ((u >> 16) & 1u); return (bf16_t)(u >> 16); }
; __device__ __forceinline__ float frsq(float x) { return __builtin_amdgcn_rsqf(x); }
; __device__ __forceinline__ float row_sum16(float v) {
;     v = dpp_add<0xB1, 0xF>(v); v = dpp_add<0x4E, 0xF>(v); v = dpp_add<0x141, 0xF>(v); v = dpp_add<0x140, 0xF>(v); return v;
; }
; __device__ __forceinline__ float wave_sum(float v) {
;     v = row_sum16(v); v = dpp_add<0x142, 0xA>(v); v = dpp_add<0x143, 0xC>(v);
;     return __int_as_float(__builtin_amdgcn_readlane(__float_as_int(v), 63));
; }
; __device__ __forceinline__ float half_sum32(float v) {
;     v = row_sum16(v); v = dpp_add<0x142, 0xA>(v);
;     const float lo = __int_as_float(__builtin_amdgcn_readlane(__float_as_int(v), 31)), hi = __int_as_float(__builtin_amdgcn_readlane(__float_as_int(v), 63));
;     return (__builtin_amdgcn_mbcnt_hi(~0u, __builtin_amdgcn_mbcnt_lo(~0u, 0u)) < 32u) ? lo : hi;
; }
; __device__ __forceinline__ void r4_zero_state(const Params& p, int l, unsigned char* ws, unsigned char* ob, int bh, int lane) {
;     ...
;         for (int r = 0; r < 16; ++r) { const int t = 32 * rb + (r & 3) + 8 * (r >> 2) + 4 * hi; const size_t row = (size_t)b * LT + t;
;             const float y0 = bf2f(y0s[r]), y1 = bf2f(y1s[r]);
;             const float mean = half_sum32(y0 + y1) * (1.f / 64.f); const float d0 = y0 - mean, d1 = y1 - mean;
;             const float var = half_sum32(d0 * d0 + d1 * d1) * (1.f / 64.f); const float rs = frsq(var + 64e-5f);
;             const float o0 = (d0 * rs * lg0 + lb0 + bcv[r] * bf2f(v0[r])) * bf2f(g0[r]);
;             const float o1 = (d1 * rs * lg1 + lb1 + bcv[r] * bf2f(v1[r])) * bf2f(g1[r]);
;             MIX[row * D + M_C + h * 64 + l31] = f2bf(o0); MIX[row * D + M_C + h * 64 + 32 + l31] = f2bf(o1); }
	v_lshlrev_b32_e32 v19, 16, v95
	v_add_f32_e32 v20, v18, v19
	v_mov_b32_e32 v21, v1
	s_nop 0
	v_add_f32_dpp v20, v20, v20 quad_perm:[1,0,3,2] row_mask:0xf bank_mask:0xf bound_ctrl:1
	s_nop 1
	v_add_f32_dpp v20, v20, v20 quad_perm:[2,3,0,1] row_mask:0xf bank_mask:0xf bound_ctrl:1
	s_nop 1
	v_add_f32_dpp v20, v20, v20 row_half_mirror row_mask:0xf bank_mask:0xf bound_ctrl:1
	s_nop 1
	v_add_f32_dpp v20, v20, v20 row_mirror row_mask:0xf bank_mask:0xf bound_ctrl:1
	s_nop 1
	v_mov_b32_dpp v21, v20 row_bcast:15 row_mask:0xa bank_mask:0xf
	v_add_f32_e32 v20, v20, v21
	s_nop 0
	v_readlane_b32 s10, v20, 31
	v_readlane_b32 s11, v20, 63
	s_nop 0
	v_mov_b32_e32 v21, s10
	v_mov_b32_e32 v20, s11
	v_cndmask_b32_e64 v20, v20, v21, s[2:3]
	v_fmac_f32_e32 v19, 0xbc800000, v20
	v_fmac_f32_e32 v18, 0xbc800000, v20
	v_mul_f32_e32 v20, v19, v19
	v_fmac_f32_e32 v20, v18, v18
	v_mov_b32_e32 v21, v1
	s_nop 0
	v_add_f32_dpp v20, v20, v20 quad_perm:[1,0,3,2] row_mask:0xf bank_mask:0xf bound_ctrl:1
	s_nop 1
	v_add_f32_dpp v20, v20, v20 quad_perm:[2,3,0,1] row_mask:0xf bank_mask:0xf bound_ctrl:1
	s_nop 1
	v_add_f32_dpp v20, v20, v20 row_half_mirror row_mask:0xf bank_mask:0xf bound_ctrl:1
	s_nop 1
	v_add_f32_dpp v20, v20, v20 row_mirror row_mask:0xf bank_mask:0xf bound_ctrl:1
	s_nop 1
	v_mov_b32_dpp v21, v20 row_bcast:15 row_mask:0xa bank_mask:0xf
	v_add_f32_e32 v20, v20, v21
	s_nop 0
	v_readlane_b32 s10, v20, 31
	v_readlane_b32 s11, v20, 63
	s_nop 0
	v_mov_b32_e32 v21, s10
	v_mov_b32_e32 v20, s11
	v_cndmask_b32_e64 v20, v20, v21, s[2:3]
	v_fmamk_f32 v20, v20, 0x3c800000, v249
	v_rsq_f32_e32 v20, v20
	s_waitcnt vmcnt(53)
	v_lshlrev_b32_e32 v21, 16, v92
	v_mul_f32_e32 v18, v18, v20
	v_fma_f32 v18, v70, v18, v72
	v_mul_f32_e32 v19, v19, v20
	v_fmac_f32_e32 v18, v81, v21
	s_waitcnt vmcnt(52)
	v_lshlrev_b32_e32 v21, 16, v91
	v_fma_f32 v19, v71, v19, v73
	s_waitcnt vmcnt(51)
	v_lshlrev_b32_e32 v20, 16, v90
	v_mul_f32_e32 v18, v18, v21
	v_fmac_f32_e32 v19, v81, v20
	s_waitcnt vmcnt(50)
	v_lshlrev_b32_e32 v20, 16, v89
	v_mul_f32_e32 v19, v19, v20
	v_bfe_u32 v20, v18, 16, 1
	v_add3_u32 v18, v18, v20, s79
	global_store_short_d16_hi v[16:17], v18, off offset:1024
	v_bfe_u32 v18, v19, 16, 1
	v_add3_u32 v18, v19, v18, s79
	global_store_short_d16_hi v[16:17], v18, off offset:1088
	s_waitcnt vmcnt(51)
	v_lshlrev_b32_e32 v16, 16, v87
	s_waitcnt vmcnt(50)
	v_lshlrev_b32_e32 v17, 16, v88
	v_add_f32_e32 v18, v16, v17
	v_mov_b32_e32 v19, v1
	s_nop 0
	v_add_f32_dpp v18, v18, v18 quad_perm:[1,0,3,2] row_mask:0xf bank_mask:0xf bound_ctrl:1
	s_nop 1
	v_add_f32_dpp v18, v18, v18 quad_perm:[2,3,0,1] row_mask:0xf bank_mask:0xf bound_ctrl:1
	s_nop 1
	v_add_f32_dpp v18, v18, v18 row_half_mirror row_mask:0xf bank_mask:0xf bound_ctrl:1
	s_nop 1
	v_add_f32_dpp v18, v18, v18 row_mirror row_mask:0xf bank_mask:0xf bound_ctrl:1
	s_nop 1
	v_mov_b32_dpp v19, v18 row_bcast:15 row_mask:0xa bank_mask:0xf
	v_add_f32_e32 v18, v18, v19
	s_nop 0
	v_readlane_b32 s10, v18, 31
	v_readlane_b32 s11, v18, 63
	s_nop 0
	v_mov_b32_e32 v19, s10
	v_mov_b32_e32 v18, s11
	v_cndmask_b32_e64 v18, v18, v19, s[2:3]
	v_fmac_f32_e32 v17, 0xbc800000, v18
	v_fmac_f32_e32 v16, 0xbc800000, v18
	v_mul_f32_e32 v18, v17, v17
	v_fmac_f32_e32 v18, v16, v16
	v_mov_b32_e32 v19, v1
	s_nop 0
	v_add_f32_dpp v18, v18, v18 quad_perm:[1,0,3,2] row_mask:0xf bank_mask:0xf bound_ctrl:1
	s_nop 1
	v_add_f32_dpp v18, v18, v18 quad_perm:[2,3,0,1] row_mask:0xf bank_mask:0xf bound_ctrl:1
	s_nop 1
	v_add_f32_dpp v18, v18, v18 row_half_mirror row_mask:0xf bank_mask:0xf bound_ctrl:1
	s_nop 1
	v_add_f32_dpp v18, v18, v18 row_mirror row_mask:0xf bank_mask:0xf bound_ctrl:1
	s_nop 1
	v_mov_b32_dpp v19, v18 row_bcast:15 row_mask:0xa bank_mask:0xf
	v_add_f32_e32 v18, v18, v19
	s_nop 0
	v_readlane_b32 s10, v18, 31
	v_readlane_b32 s11, v18, 63
	s_nop 0
	v_mov_b32_e32 v19, s10
	v_mov_b32_e32 v18, s11
	v_cndmask_b32_e64 v18, v18, v19, s[2:3]
	v_fmamk_f32 v18, v18, 0x3c800000, v249
	v_rsq_f32_e32 v18, v18
	s_waitcnt vmcnt(49)
	v_lshlrev_b32_e32 v19, 16, v85
	v_mul_f32_e32 v16, v16, v18
	v_fma_f32 v16, v70, v16, v72
	v_mul_f32_e32 v17, v17, v18
	v_fmac_f32_e32 v16, v80, v19
	s_waitcnt vmcnt(48)
	v_lshlrev_b32_e32 v19, 16, v84
	v_fma_f32 v17, v71, v17, v73
	s_waitcnt vmcnt(47)
	v_lshlrev_b32_e32 v18, 16, v83
	v_mul_f32_e32 v16, v16, v19
	v_fmac_f32_e32 v17, v80, v18
	s_waitcnt vmcnt(46)
	v_lshlrev_b32_e32 v18, 16, v60
	v_mul_f32_e32 v17, v17, v18
	v_bfe_u32 v18, v16, 16, 1
	v_add3_u32 v16, v16, v18, s79
	global_store_short_d16_hi v[14:15], v16, off offset:1024
	v_bfe_u32 v16, v17, 16, 1
	v_add3_u32 v16, v17, v16, s79
	global_store_short_d16_hi v[14:15], v16, off offset:1088
	s_waitcnt vmcnt(47)
	v_lshlrev_b32_e32 v14, 16, v58
	s_waitcnt vmcnt(46)
	v_lshlrev_b32_e32 v15, 16, v59
	v_add_f32_e32 v16, v14, v15
	v_mov_b32_e32 v17, v1
	s_nop 0
	v_add_f32_dpp v16, v16, v16 quad_perm:[1,0,3,2] row_mask:0xf bank_mask:0xf bound_ctrl:1
	s_nop 1
	v_add_f32_dpp v16, v16, v16 quad_perm:[2,3,0,1] row_mask:0xf bank_mask:0xf bound_ctrl:1
	s_nop 1
	v_add_f32_dpp v16, v16, v16 row_half_mirror row_mask:0xf bank_mask:0xf bound_ctrl:1
	s_nop 1
	v_add_f32_dpp v16, v16, v16 row_mirror row_mask:0xf bank_mask:0xf bound_ctrl:1
	s_nop 1
	v_mov_b32_dpp v17, v16 row_bcast:15 row_mask:0xa bank_mask:0xf
	v_add_f32_e32 v16, v16, v17
	s_nop 0
	v_readlane_b32 s10, v16, 31
	v_readlane_b32 s11, v16, 63
	s_nop 0
	v_mov_b32_e32 v17, s10
	v_mov_b32_e32 v16, s11
	v_cndmask_b32_e64 v16, v16, v17, s[2:3]
	v_fmac_f32_e32 v15, 0xbc800000, v16
	v_fmac_f32_e32 v14, 0xbc800000, v16
	v_mul_f32_e32 v16, v15, v15
	v_fmac_f32_e32 v16, v14, v14
	v_mov_b32_e32 v17, v1
	s_nop 0
	v_add_f32_dpp v16, v16, v16 quad_perm:[1,0,3,2] row_mask:0xf bank_mask:0xf bound_ctrl:1
	s_nop 1
	v_add_f32_dpp v16, v16, v16 quad_perm:[2,3,0,1] row_mask:0xf bank_mask:0xf bound_ctrl:1
	s_nop 1
	v_add_f32_dpp v16, v16, v16 row_half_mirror row_mask:0xf bank_mask:0xf bound_ctrl:1
	s_nop 1
	v_add_f32_dpp v16, v16, v16 row_mirror row_mask:0xf bank_mask:0xf bound_ctrl:1
	s_nop 1
	v_mov_b32_dpp v17, v16 row_bcast:15 row_mask:0xa bank_mask:0xf
	v_add_f32_e32 v16, v16, v17
	s_nop 0
	v_readlane_b32 s10, v16, 31
	v_readlane_b32 s11, v16, 63
	s_nop 0
	v_mov_b32_e32 v17, s10
	v_mov_b32_e32 v16, s11
	v_cndmask_b32_e64 v16, v16, v17, s[2:3]
	v_fmamk_f32 v16, v16, 0x3c800000, v249
	v_rsq_f32_e32 v16, v16
	s_waitcnt vmcnt(45)
; __device__ __forceinline__ float bf2f(bf16_t b) { return __uint_as_float(((unsigned)b) << 16); }
; __device__ __forceinline__ bf16_t f2bf(float f) { unsigned u = __float_as_uint(f); u += 0x7FFFu + ((u >> 16) & 1u); return (bf16_t)(u >> 16); }
; __device__ __forceinline__ float frsq(float x) { return __builtin_amdgcn_rsqf(x); }
; __device__ __forceinline__ float row_sum16(float v) {
;     v = dpp_add<0xB1, 0xF>(v); v = dpp_add<0x4E, 0xF>(v); v = dpp_add<0x141, 0xF>(v); v = dpp_add<0x140, 0xF>(v); return v;
; }
; __device__ __forceinline__ float wave_sum(float v) {
;     v = row_sum16(v); v = dpp_add<0x142, 0xA>(v); v = dpp_add<0x143, 0xC>(v);
;     return __int_as_float(__builtin_amdgcn_readlane(__float_as_int(v), 63));
; }
; __device__ __forceinline__ float half_sum32(float v) {
;     v = row_sum16(v); v = dpp_add<0x142, 0xA>(v);
;     const float lo = __int_as_float(__builtin_amdgcn_readlane(__float_as_int(v), 31)), hi = __int_as_float(__builtin_amdgcn_readlane(__float_as_int(v), 63));
;     return (__builtin_amdgcn_mbcnt_hi(~0u, __builtin_amdgcn_mbcnt_lo(~0u, 0u)) < 32u) ? lo : hi;
; }
; __device__ __forceinline__ void r4_zero_state(const Params& p, int l, unsigned char* ws, unsigned char* ob, int bh, int lane) {
;     ...
;         for (int r = 0; r < 16; ++r) { const int t = 32 * rb + (r & 3) + 8 * (r >> 2) + 4 * hi; const size_t row = (size_t)b * LT + t;
;             const float y0 = bf2f(y0s[r]), y1 = bf2f(y1s[r]);
;             const float mean = half_sum32(y0 + y1) * (1.f / 64.f); const float d0 = y0 - mean, d1 = y1 - mean;
;             const float var = half_sum32(d0 * d0 + d1 * d1) * (1.f / 64.f); const float rs = frsq(var + 64e-5f);
;             const float o0 = (d0 * rs * lg0 + lb0 + bcv[r] * bf2f(v0[r])) * bf2f(g0[r]);
;             const float o1 = (d1 * rs * lg1 + lb1 + bcv[r] * bf2f(v1[r])) * bf2f(g1[r]);
;             MIX[row * D + M_C + h * 64 + l31] = f2bf(o0); MIX[row * D + M_C + h * 64 + 32 + l31] = f2bf(o1); }
	v_lshlrev_b32_e32 v17, 16, v57
	v_mul_f32_e32 v14, v14, v16
	v_fma_f32 v14, v70, v14, v72
	v_mul_f32_e32 v15, v15, v16
	v_fmac_f32_e32 v14, v79, v17
	s_waitcnt vmcnt(44)
	v_lshlrev_b32_e32 v17, 16, v56
	v_fma_f32 v15, v71, v15, v73
	s_waitcnt vmcnt(43)
	v_lshlrev_b32_e32 v16, 16, v55
	v_mul_f32_e32 v14, v14, v17
	v_fmac_f32_e32 v15, v79, v16
	s_waitcnt vmcnt(42)
	v_lshlrev_b32_e32 v16, 16, v54
	v_mul_f32_e32 v15, v15, v16
	v_bfe_u32 v16, v14, 16, 1
	v_add3_u32 v14, v14, v16, s79
	global_store_short_d16_hi v[12:13], v14, off offset:1024
	v_bfe_u32 v14, v15, 16, 1
	v_add3_u32 v14, v15, v14, s79
	global_store_short_d16_hi v[12:13], v14, off offset:1088
	s_waitcnt vmcnt(43)
	v_lshlrev_b32_e32 v12, 16, v52
	s_waitcnt vmcnt(42)
	v_lshlrev_b32_e32 v13, 16, v53
	v_add_f32_e32 v14, v12, v13
	v_mov_b32_e32 v15, v1
	s_nop 0
	v_add_f32_dpp v14, v14, v14 quad_perm:[1,0,3,2] row_mask:0xf bank_mask:0xf bound_ctrl:1
	s_nop 1
	v_add_f32_dpp v14, v14, v14 quad_perm:[2,3,0,1] row_mask:0xf bank_mask:0xf bound_ctrl:1
	s_nop 1
	v_add_f32_dpp v14, v14, v14 row_half_mirror row_mask:0xf bank_mask:0xf bound_ctrl:1
	s_nop 1
	v_add_f32_dpp v14, v14, v14 row_mirror row_mask:0xf bank_mask:0xf bound_ctrl:1
	s_nop 1
	v_mov_b32_dpp v15, v14 row_bcast:15 row_mask:0xa bank_mask:0xf
	v_add_f32_e32 v14, v14, v15
	s_nop 0
	v_readlane_b32 s10, v14, 31
	v_readlane_b32 s11, v14, 63
	s_nop 0
	v_mov_b32_e32 v15, s10
	v_mov_b32_e32 v14, s11
	v_cndmask_b32_e64 v14, v14, v15, s[2:3]
	v_fmac_f32_e32 v13, 0xbc800000, v14
	v_fmac_f32_e32 v12, 0xbc800000, v14
	v_mul_f32_e32 v14, v13, v13
	v_fmac_f32_e32 v14, v12, v12
	v_mov_b32_e32 v15, v1
	s_nop 0
	v_add_f32_dpp v14, v14, v14 quad_perm:[1,0,3,2] row_mask:0xf bank_mask:0xf bound_ctrl:1
	s_nop 1
	v_add_f32_dpp v14, v14, v14 quad_perm:[2,3,0,1] row_mask:0xf bank_mask:0xf bound_ctrl:1
	s_nop 1
	v_add_f32_dpp v14, v14, v14 row_half_mirror row_mask:0xf bank_mask:0xf bound_ctrl:1
	s_nop 1
	v_add_f32_dpp v14, v14, v14 row_mirror row_mask:0xf bank_mask:0xf bound_ctrl:1
	s_nop 1
	v_mov_b32_dpp v15, v14 row_bcast:15 row_mask:0xa bank_mask:0xf
	v_add_f32_e32 v14, v14, v15
	s_nop 0
	v_readlane_b32 s10, v14, 31
	v_readlane_b32 s11, v14, 63
	s_nop 0
	v_mov_b32_e32 v15, s10
	v_mov_b32_e32 v14, s11
	v_cndmask_b32_e64 v14, v14, v15, s[2:3]
	v_fmamk_f32 v14, v14, 0x3c800000, v249
	v_rsq_f32_e32 v14, v14
	s_waitcnt vmcnt(41)
	v_lshlrev_b32_e32 v15, 16, v51
	v_mul_f32_e32 v12, v12, v14
	v_fma_f32 v12, v70, v12, v72
	v_mul_f32_e32 v13, v13, v14
	v_fmac_f32_e32 v12, v78, v15
	s_waitcnt vmcnt(40)
	v_lshlrev_b32_e32 v15, 16, v50
	v_fma_f32 v13, v71, v13, v73
	s_waitcnt vmcnt(39)
	v_lshlrev_b32_e32 v14, 16, v49
	v_mul_f32_e32 v12, v12, v15
	v_fmac_f32_e32 v13, v78, v14
	s_waitcnt vmcnt(38)
	v_lshlrev_b32_e32 v14, 16, v48
	v_mul_f32_e32 v13, v13, v14
	v_bfe_u32 v14, v12, 16, 1
	v_add3_u32 v12, v12, v14, s79
	global_store_short_d16_hi v[10:11], v12, off offset:1024
	v_bfe_u32 v12, v13, 16, 1
	v_add3_u32 v12, v13, v12, s79
	global_store_short_d16_hi v[10:11], v12, off offset:1088
	s_waitcnt vmcnt(39)
	v_lshlrev_b32_e32 v10, 16, v46
	s_waitcnt vmcnt(38)
; __device__ __forceinline__ float bf2f(bf16_t b) { return __uint_as_float(((unsigned)b) << 16); }
; __device__ __forceinline__ bf16_t f2bf(float f) { unsigned u = __float_as_uint(f); u += 0x7FFFu + ((u >> 16) & 1u); return (bf16_t)(u >> 16); }
; __device__ __forceinline__ float frsq(float x) { return __builtin_amdgcn_rsqf(x); }
; __device__ __forceinline__ float row_sum16(float v) {
;     v = dpp_add<0xB1, 0xF>(v); v = dpp_add<0x4E, 0xF>(v); v = dpp_add<0x141, 0xF>(v); v = dpp_add<0x140, 0xF>(v); return v;
; }
; __device__ __forceinline__ float wave_sum(float v) {
;     v = row_sum16(v); v = dpp_add<0x142, 0xA>(v); v = dpp_add<0x143, 0xC>(v);
;     return __int_as_float(__builtin_amdgcn_readlane(__float_as_int(v), 63));
; }
; __device__ __forceinline__ float half_sum32(float v) {
;     v = row_sum16(v); v = dpp_add<0x142, 0xA>(v);
;     const float lo = __int_as_float(__builtin_amdgcn_readlane(__float_as_int(v), 31)), hi = __int_as_float(__builtin_amdgcn_readlane(__float_as_int(v), 63));
;     return (__builtin_amdgcn_mbcnt_hi(~0u, __builtin_amdgcn_mbcnt_lo(~0u, 0u)) < 32u) ? lo : hi;
; }
; __device__ __forceinline__ void r4_zero_state(const Params& p, int l, unsigned char* ws, unsigned char* ob, int bh, int lane) {
;     ...
;         for (int r = 0; r < 16; ++r) { const int t = 32 * rb + (r & 3) + 8 * (r >> 2) + 4 * hi; const size_t row = (size_t)b * LT + t;
;             const float y0 = bf2f(y0s[r]), y1 = bf2f(y1s[r]);
;             const float mean = half_sum32(y0 + y1) * (1.f / 64.f); const float d0 = y0 - mean, d1 = y1 - mean;
;             const float var = half_sum32(d0 * d0 + d1 * d1) * (1.f / 64.f); const float rs = frsq(var + 64e-5f);
;             const float o0 = (d0 * rs * lg0 + lb0 + bcv[r] * bf2f(v0[r])) * bf2f(g0[r]);
;             const float o1 = (d1 * rs * lg1 + lb1 + bcv[r] * bf2f(v1[r])) * bf2f(g1[r]);
;             MIX[row * D + M_C + h * 64 + l31] = f2bf(o0); MIX[row * D + M_C + h * 64 + 32 + l31] = f2bf(o1); }
	v_lshlrev_b32_e32 v11, 16, v47
	v_add_f32_e32 v12, v10, v11
	v_mov_b32_e32 v13, v1
	s_nop 0
	v_add_f32_dpp v12, v12, v12 quad_perm:[1,0,3,2] row_mask:0xf bank_mask:0xf bound_ctrl:1
	s_nop 1
	v_add_f32_dpp v12, v12, v12 quad_perm:[2,3,0,1] row_mask:0xf bank_mask:0xf bound_ctrl:1
	s_nop 1
	v_add_f32_dpp v12, v12, v12 row_half_mirror row_mask:0xf bank_mask:0xf bound_ctrl:1
	s_nop 1
	v_add_f32_dpp v12, v12, v12 row_mirror row_mask:0xf bank_mask:0xf bound_ctrl:1
	s_nop 1
	v_mov_b32_dpp v13, v12 row_bcast:15 row_mask:0xa bank_mask:0xf
	v_add_f32_e32 v12, v12, v13
	s_nop 0
	v_readlane_b32 s10, v12, 31
	v_readlane_b32 s11, v12, 63
	s_nop 0
	v_mov_b32_e32 v13, s10
	v_mov_b32_e32 v12, s11
	v_cndmask_b32_e64 v12, v12, v13, s[2:3]
	v_fmac_f32_e32 v11, 0xbc800000, v12
	v_fmac_f32_e32 v10, 0xbc800000, v12
	v_mul_f32_e32 v12, v11, v11
	v_fmac_f32_e32 v12, v10, v10
	v_mov_b32_e32 v13, v1
	s_nop 0
	v_add_f32_dpp v12, v12, v12 quad_perm:[1,0,3,2] row_mask:0xf bank_mask:0xf bound_ctrl:1
	s_nop 1
	v_add_f32_dpp v12, v12, v12 quad_perm:[2,3,0,1] row_mask:0xf bank_mask:0xf bound_ctrl:1
	s_nop 1
	v_add_f32_dpp v12, v12, v12 row_half_mirror row_mask:0xf bank_mask:0xf bound_ctrl:1
	s_nop 1
	v_add_f32_dpp v12, v12, v12 row_mirror row_mask:0xf bank_mask:0xf bound_ctrl:1
	s_nop 1
	v_mov_b32_dpp v13, v12 row_bcast:15 row_mask:0xa bank_mask:0xf
	v_add_f32_e32 v12, v12, v13
	s_nop 0
	v_readlane_b32 s10, v12, 31
	v_readlane_b32 s11, v12, 63
	s_nop 0
	v_mov_b32_e32 v13, s10
	v_mov_b32_e32 v12, s11
	v_cndmask_b32_e64 v12, v12, v13, s[2:3]
	v_fmamk_f32 v12, v12, 0x3c800000, v249
	v_rsq_f32_e32 v12, v12
	s_waitcnt vmcnt(37)
	v_lshlrev_b32_e32 v13, 16, v45
	v_mul_f32_e32 v10, v10, v12
	v_fma_f32 v10, v70, v10, v72
	v_mul_f32_e32 v11, v11, v12
	v_fmac_f32_e32 v10, v77, v13
	s_waitcnt vmcnt(36)
	v_lshlrev_b32_e32 v13, 16, v44
	v_fma_f32 v11, v71, v11, v73
	s_waitcnt vmcnt(35)
	v_lshlrev_b32_e32 v12, 16, v43
	v_mul_f32_e32 v10, v10, v13
	v_fmac_f32_e32 v11, v77, v12
	s_waitcnt vmcnt(34)
	v_lshlrev_b32_e32 v12, 16, v42
	v_mul_f32_e32 v11, v11, v12
	v_bfe_u32 v12, v10, 16, 1
	v_add3_u32 v10, v10, v12, s79
	global_store_short_d16_hi v[8:9], v10, off offset:1024
	v_bfe_u32 v10, v11, 16, 1
	v_add3_u32 v10, v11, v10, s79
	global_store_short_d16_hi v[8:9], v10, off offset:1088
	s_waitcnt vmcnt(35)
	v_lshlrev_b32_e32 v8, 16, v40
	s_waitcnt vmcnt(34)
	v_lshlrev_b32_e32 v9, 16, v41
	v_add_f32_e32 v10, v8, v9
	v_mov_b32_e32 v11, v1
	s_nop 0
	v_add_f32_dpp v10, v10, v10 quad_perm:[1,0,3,2] row_mask:0xf bank_mask:0xf bound_ctrl:1
	s_nop 1
	v_add_f32_dpp v10, v10, v10 quad_perm:[2,3,0,1] row_mask:0xf bank_mask:0xf bound_ctrl:1
	s_nop 1
	v_add_f32_dpp v10, v10, v10 row_half_mirror row_mask:0xf bank_mask:0xf bound_ctrl:1
	s_nop 1
	v_add_f32_dpp v10, v10, v10 row_mirror row_mask:0xf bank_mask:0xf bound_ctrl:1
	s_nop 1
	v_mov_b32_dpp v11, v10 row_bcast:15 row_mask:0xa bank_mask:0xf
	v_add_f32_e32 v10, v10, v11
	s_nop 0
	v_readlane_b32 s10, v10, 31
	v_readlane_b32 s11, v10, 63
	s_nop 0
	v_mov_b32_e32 v11, s10
	v_mov_b32_e32 v10, s11
	v_cndmask_b32_e64 v10, v10, v11, s[2:3]
	v_fmac_f32_e32 v9, 0xbc800000, v10
	v_fmac_f32_e32 v8, 0xbc800000, v10
	v_mul_f32_e32 v10, v9, v9
	v_fmac_f32_e32 v10, v8, v8
	v_mov_b32_e32 v11, v1
	s_nop 0
	v_add_f32_dpp v10, v10, v10 quad_perm:[1,0,3,2] row_mask:0xf bank_mask:0xf bound_ctrl:1
	s_nop 1
	v_add_f32_dpp v10, v10, v10 quad_perm:[2,3,0,1] row_mask:0xf bank_mask:0xf bound_ctrl:1
	s_nop 1
	v_add_f32_dpp v10, v10, v10 row_half_mirror row_mask:0xf bank_mask:0xf bound_ctrl:1
	s_nop 1
	v_add_f32_dpp v10, v10, v10 row_mirror row_mask:0xf bank_mask:0xf bound_ctrl:1
	s_nop 1
	v_mov_b32_dpp v11, v10 row_bcast:15 row_mask:0xa bank_mask:0xf
	v_add_f32_e32 v10, v10, v11
	s_nop 0
	v_readlane_b32 s10, v10, 31
	v_readlane_b32 s11, v10, 63
	s_nop 0
	v_mov_b32_e32 v11, s10
	v_mov_b32_e32 v10, s11
	v_cndmask_b32_e64 v10, v10, v11, s[2:3]
	v_fmamk_f32 v10, v10, 0x3c800000, v249
	v_rsq_f32_e32 v10, v10
	s_waitcnt vmcnt(33)
	v_lshlrev_b32_e32 v11, 16, v39
	s_mov_b64 s[10:11], 0
	v_mul_f32_e32 v8, v8, v10
	v_fma_f32 v8, v70, v8, v72
	v_mul_f32_e32 v9, v9, v10
	v_fmac_f32_e32 v8, v0, v11
	s_waitcnt vmcnt(32)
	v_lshlrev_b32_e32 v11, 16, v38
	v_fma_f32 v9, v71, v9, v73
	s_waitcnt vmcnt(31)
	v_lshlrev_b32_e32 v10, 16, v37
	v_mul_f32_e32 v8, v8, v11
	v_fmac_f32_e32 v9, v0, v10
	s_waitcnt vmcnt(30)
	v_lshlrev_b32_e32 v0, 16, v36
	v_mul_f32_e32 v0, v9, v0
	v_bfe_u32 v9, v8, 16, 1
	v_add3_u32 v8, v8, v9, s79
	global_store_short_d16_hi v[6:7], v8, off offset:1024
	v_bfe_u32 v8, v0, 16, 1
	v_add3_u32 v0, v0, v8, s79
	global_store_short_d16_hi v[6:7], v0, off offset:1088
	s_cbranch_vccz .LBB0_759

; #define LAS __attribute__((address_space(3)))
; __device__ __forceinline__ unsigned pk2(float lo, float hi) { return (unsigned)f2bf(lo) | ((unsigned)f2bf(hi) << 16); }
; __device__ __forceinline__ float frsq(float x) { return __builtin_amdgcn_rsqf(x); }
; __device__ __forceinline__ void ln_affine(f32x4 (&v)[4], const LnPar& q) {
;     float s = 0.f;
; #pragma unroll
;     for (int j = 0; j < 4; ++j) s += (v[j][0] + v[j][1]) + (v[j][2] + v[j][3]);
;     const float mean = wave_sum(s) * (1.f / D); float s2 = 0.f;
; #pragma unroll
;     for (int j = 0; j < 4; ++j) { v[j] = v[j] - mean; s2 += (v[j][0] * v[j][0] + v[j][1] * v[j][1]) + (v[j][2] * v[j][2] + v[j][3] * v[j][3]); }
;     const float rstd = frsq(wave_sum(s2) * (1.f / D) + 1e-5f);
; #pragma unroll
;     for (int j = 0; j < 4; ++j) v[j] = v[j] * rstd * q.g[j] + q.b[j];
; }
; __device__ __forceinline__ void store_row_bf16(bf16_t* row, const f32x4 (&v)[4], int lane) {
; #pragma unroll
;     for (int j = 0; j < 4; ++j) { u32x2 w; w.x = pk2(v[j][0], v[j][1]); w.y = pk2(v[j][2], v[j][3]); *(u32x2*)(row + 4 * lane + 256 * j) = w; }
; }
; __device__ __forceinline__ void ph_ln1(const Params& p, int l, LAS unsigned char* lds, const int wvid) {
;     ...
;         ln_affine(v, ln1);
;         store_row_bf16(HB + (size_t)r * D, v, lane);
;         float lg[16];
; #pragma unroll
;         for (int e = 0; e < 16; ++e) lg[e] = 0.f;
; #pragma unroll
;         for (int j = 0; j < 4; ++j)
; #pragma unroll
;             for (int e = 0; e < 16; ++e) { const f32x4 w = *(const LAS f32x4*)(rw + e * D + 256 * j + 4 * lane);
.LBB0_1078:
	s_or_b64 exec, exec, s[0:1]
	v_pk_add_f32 v[64:65], v[66:67], v[34:35]
	v_add_f32_e32 v75, v62, v63
	v_add_f32_e32 v0, v64, v65
	v_pk_add_f32 v[64:65], v[68:69], v[36:37]
	v_add_f32_e32 v77, 0, v0
	v_pk_add_f32 v[64:65], v[64:65], v[64:65] op_sel_hi:[0,1]
	v_add_f32_e32 v79, v60, v61
	v_mov_b32_e32 v73, v65
	v_pk_add_f32 v[70:71], v[74:75], v[78:79]
	v_pk_add_f32 v[64:65], v[72:73], v[76:77]
	ds_read_b128 v[118:121], v39
	ds_read_b128 v[122:125], v39 offset:4096
	ds_read_b128 v[126:129], v39 offset:8192
	ds_read_b128 v[130:133], v39 offset:12288
	ds_read_b128 v[134:137], v39 offset:16384
	ds_read_b128 v[138:141], v39 offset:20480
	ds_read_b128 v[142:145], v39 offset:24576
	ds_read_b128 v[146:149], v39 offset:28672
	ds_read_b128 v[232:235], v39 offset:32768
	ds_read_b128 v[236:239], v39 offset:36864
	ds_read_b128 v[240:243], v39 offset:40960
	ds_read_b128 v[244:247], v39 offset:45056
	v_pk_add_f32 v[64:65], v[70:71], v[64:65]
	s_nop 0
	v_add_f32_e32 v0, v64, v65
	v_mov_b32_e32 v64, v1
	s_nop 0
	v_add_f32_dpp v0, v0, v0 quad_perm:[1,0,3,2] row_mask:0xf bank_mask:0xf bound_ctrl:1
	s_nop 1
	v_add_f32_dpp v0, v0, v0 quad_perm:[2,3,0,1] row_mask:0xf bank_mask:0xf bound_ctrl:1
	s_nop 1
	v_add_f32_dpp v0, v0, v0 row_half_mirror row_mask:0xf bank_mask:0xf bound_ctrl:1
	s_nop 1
	v_add_f32_dpp v0, v0, v0 row_mirror row_mask:0xf bank_mask:0xf bound_ctrl:1
	s_nop 1
	v_mov_b32_dpp v64, v0 row_bcast:15 row_mask:0xa bank_mask:0xf
	v_add_f32_e32 v0, v0, v64
	v_mov_b32_e32 v64, v1
	s_nop 1
	v_mov_b32_dpp v64, v0 row_bcast:31 row_mask:0xc bank_mask:0xf
	v_add_f32_e32 v0, v0, v64
	s_nop 0
	v_readlane_b32 s0, v0, 63
	s_nop 1
	v_fmac_f32_e32 v66, s0, v220
	v_fmac_f32_e32 v35, s0, v220
	v_fmac_f32_e32 v67, s0, v220
	v_fmac_f32_e32 v34, s0, v220
	v_mov_b32_e32 v64, v67
	v_mov_b32_e32 v65, v35
	v_mov_b32_e32 v35, v66
	v_pk_mul_f32 v[70:71], v[64:65], v[64:65]
	v_pk_mul_f32 v[66:67], v[34:35], v[34:35]
	v_fmac_f32_e32 v68, s0, v220
	v_fmac_f32_e32 v37, s0, v220
	v_fmac_f32_e32 v69, s0, v220
	v_pk_mov_b32 v[80:81], v[66:67], v[70:71] op_sel:[1,0]
	v_mov_b32_e32 v67, v71
	v_fmac_f32_e32 v36, s0, v220
	v_mov_b32_e32 v70, v69
	v_mov_b32_e32 v71, v37
	v_mov_b32_e32 v37, v68
	v_pk_add_f32 v[66:67], v[80:81], v[66:67]
	v_pk_mul_f32 v[80:81], v[70:71], v[70:71]
	v_pk_mul_f32 v[68:69], v[36:37], v[36:37]
	v_fmac_f32_e32 v62, s0, v220
	v_pk_mov_b32 v[82:83], v[68:69], v[80:81] op_sel:[1,0]
	v_mov_b32_e32 v69, v81
	v_fmac_f32_e32 v63, s0, v220
	v_fmac_f32_e32 v60, s0, v220
	v_mul_f32_e32 v0, v62, v62
	v_pk_add_f32 v[68:69], v[82:83], v[68:69]
	v_fmac_f32_e32 v61, s0, v220
	v_pk_fma_f32 v[80:81], v[62:63], v[62:63], v[0:1] op_sel_hi:[1,1,0]
	v_mul_f32_e32 v0, v60, v60
	v_pk_add_f32 v[66:67], v[66:67], v[66:67] op_sel_hi:[0,1]
	v_pk_add_f32 v[68:69], v[68:69], v[68:69] op_sel_hi:[0,1]
	v_pk_fma_f32 v[82:83], v[60:61], v[60:61], v[0:1] op_sel_hi:[1,1,0]
	v_fmac_f32_e32 v76, s0, v220
	v_fmac_f32_e32 v72, s0, v220
	v_fmac_f32_e32 v78, s0, v220
	v_fmac_f32_e32 v74, s0, v220
	v_mul_f32_e32 v80, v74, v74
	v_mul_f32_e32 v82, v78, v78
	v_mul_f32_e32 v66, v72, v72
	v_mul_f32_e32 v68, v76, v76
	v_pk_add_f32 v[80:81], v[80:81], v[82:83]
	v_pk_add_f32 v[66:67], v[66:67], v[68:69]
	v_mov_b32_e32 v75, v78
	v_pk_add_f32 v[66:67], v[80:81], v[66:67]
	v_mov_b32_e32 v73, v76
	v_add_f32_e32 v0, v66, v67
	v_mov_b32_e32 v66, v1
	s_nop 0
	v_add_f32_dpp v0, v0, v0 quad_perm:[1,0,3,2] row_mask:0xf bank_mask:0xf bound_ctrl:1
	s_nop 1
	v_add_f32_dpp v0, v0, v0 quad_perm:[2,3,0,1] row_mask:0xf bank_mask:0xf bound_ctrl:1
	s_nop 1
	v_add_f32_dpp v0, v0, v0 row_half_mirror row_mask:0xf bank_mask:0xf bound_ctrl:1
	s_nop 1
	v_add_f32_dpp v0, v0, v0 row_mirror row_mask:0xf bank_mask:0xf bound_ctrl:1
	s_nop 1
	v_mov_b32_dpp v66, v0 row_bcast:15 row_mask:0xa bank_mask:0xf
	v_add_f32_e32 v0, v0, v66
	v_mov_b32_e32 v66, v1
	s_nop 1
	v_mov_b32_dpp v66, v0 row_bcast:31 row_mask:0xc bank_mask:0xf
	v_add_f32_e32 v0, v0, v66
	s_nop 0
	v_readlane_b32 s0, v0, 63
	s_nop 1
	v_fma_f32 v0, s0, v221, v204
	v_rsq_f32_e32 v0, v0
	s_nop 0
	v_pk_mul_f32 v[34:35], v[34:35], v[0:1] op_sel_hi:[1,0]
	s_nop 0
	v_pk_fma_f32 v[94:95], v[30:31], v[34:35], v[22:23]
	v_pk_mul_f32 v[34:35], v[36:37], v[0:1] op_sel_hi:[1,0]
	v_pk_mul_f32 v[36:37], v[70:71], v[0:1] op_sel_hi:[1,0]
	v_pk_mul_f32 v[64:65], v[64:65], v[0:1] op_sel_hi:[1,0]
	v_pk_fma_f32 v[68:69], v[28:29], v[36:37], v[20:21]
	v_pk_fma_f32 v[70:71], v[26:27], v[34:35], v[18:19]
	v_pk_mul_f32 v[34:35], v[62:63], v[0:1] op_sel_hi:[1,0]
	v_pk_mul_f32 v[36:37], v[60:61], v[0:1] op_sel_hi:[1,0]
	v_pk_fma_f32 v[92:93], v[32:33], v[64:65], v[24:25]
	v_pk_fma_f32 v[64:65], v[16:17], v[36:37], v[8:9]
	v_pk_fma_f32 v[66:67], v[14:15], v[34:35], v[6:7]
	v_pk_mul_f32 v[34:35], v[74:75], v[0:1] op_sel_hi:[1,0]
	v_pk_mul_f32 v[36:37], v[72:73], v[0:1] op_sel_hi:[1,0]
	v_bfe_u32 v0, v94, 16, 1
	v_pk_fma_f32 v[62:63], v[10:11], v[34:35], v[2:3]
	v_add3_u32 v0, v94, v0, s79
	v_bfe_u32 v34, v95, 16, 1
	v_lshrrev_b32_e32 v0, 16, v0
	v_add3_u32 v34, v95, v34, s79
	v_and_or_b32 v34, v34, s89, v0
	v_bfe_u32 v0, v92, 16, 1
	v_add3_u32 v0, v92, v0, s79
	v_bfe_u32 v35, v93, 16, 1
	v_lshrrev_b32_e32 v0, 16, v0
	v_add3_u32 v35, v93, v35, s79
	v_and_or_b32 v35, v35, s89, v0
	v_bfe_u32 v0, v70, 16, 1
	global_store_dwordx2 v[58:59], v[34:35], off offset:-1536
	v_add3_u32 v0, v70, v0, s79
	v_bfe_u32 v34, v71, 16, 1
	v_lshrrev_b32_e32 v0, 16, v0
	v_add3_u32 v34, v71, v34, s79
	v_and_or_b32 v34, v34, s89, v0
	v_bfe_u32 v0, v68, 16, 1
	v_add3_u32 v0, v68, v0, s79
	v_bfe_u32 v35, v69, 16, 1
	v_lshrrev_b32_e32 v0, 16, v0
	v_add3_u32 v35, v69, v35, s79
	v_and_or_b32 v35, v35, s89, v0
	v_bfe_u32 v0, v66, 16, 1
	global_store_dwordx2 v[58:59], v[34:35], off offset:-1024
	v_add3_u32 v0, v66, v0, s79
	v_bfe_u32 v34, v67, 16, 1
	v_lshrrev_b32_e32 v0, 16, v0
	v_add3_u32 v34, v67, v34, s79
	v_and_or_b32 v34, v34, s89, v0
	v_bfe_u32 v0, v64, 16, 1
	v_add3_u32 v0, v64, v0, s79
	v_bfe_u32 v35, v65, 16, 1
	v_lshrrev_b32_e32 v0, 16, v0
	v_add3_u32 v35, v65, v35, s79
	v_and_or_b32 v35, v35, s89, v0
	v_bfe_u32 v0, v62, 16, 1
	global_store_dwordx2 v[58:59], v[34:35], off offset:-512
	v_add3_u32 v0, v62, v0, s79
	v_bfe_u32 v34, v63, 16, 1
	v_pk_fma_f32 v[60:61], v[12:13], v[36:37], v[4:5]
	v_lshrrev_b32_e32 v0, 16, v0
	v_add3_u32 v34, v63, v34, s79
	v_and_or_b32 v34, v34, s89, v0
	v_bfe_u32 v0, v60, 16, 1
	v_add3_u32 v0, v60, v0, s79
	v_bfe_u32 v35, v61, 16, 1
	v_lshrrev_b32_e32 v0, 16, v0
	v_add3_u32 v35, v61, v35, s79
	v_and_or_b32 v35, v35, s89, v0
	global_store_dwordx2 v[58:59], v[34:35], off
	s_waitcnt lgkmcnt(11)
; #define LAS __attribute__((address_space(3)))
; __device__ __forceinline__ void ph_ln1(const Params& p, int l, LAS unsigned char* lds, const int wvid) {
;     ...
;         for (int j = 0; j < 4; ++j)
; #pragma unroll
;             for (int e = 0; e < 16; ++e) { const f32x4 w = *(const LAS f32x4*)(rw + e * D + 256 * j + 4 * lane);
;                 lg[e] += (v[j][0] * w[0] + v[j][1] * w[1]) + (v[j][2] * w[2] + v[j][3] * w[3]); }
	v_pk_mul_f32 v[196:197], v[94:95], v[118:119]
	v_pk_fma_f32 v[196:197], v[92:93], v[120:121], v[196:197]
	ds_read_b128 v[118:121], v39 offset:49152
	s_waitcnt lgkmcnt(11)
	v_pk_mul_f32 v[198:199], v[94:95], v[122:123]
	v_pk_fma_f32 v[198:199], v[92:93], v[124:125], v[198:199]
	ds_read_b128 v[122:125], v39 offset:53248
	s_waitcnt lgkmcnt(11)
	v_pk_mul_f32 v[200:201], v[94:95], v[126:127]
	v_pk_fma_f32 v[200:201], v[92:93], v[128:129], v[200:201]
	ds_read_b128 v[126:129], v39 offset:57344
	s_waitcnt lgkmcnt(11)
	v_pk_mul_f32 v[202:203], v[94:95], v[130:131]
	v_pk_fma_f32 v[202:203], v[92:93], v[132:133], v[202:203]
	ds_read_b128 v[130:133], v39 offset:61440
	s_waitcnt lgkmcnt(11)
	v_pk_mul_f32 v[206:207], v[94:95], v[134:135]
	v_pk_fma_f32 v[206:207], v[92:93], v[136:137], v[206:207]
	ds_read_b128 v[134:137], v39 offset:1024
	s_waitcnt lgkmcnt(11)
	v_pk_mul_f32 v[208:209], v[94:95], v[138:139]
	v_pk_fma_f32 v[208:209], v[92:93], v[140:141], v[208:209]
	ds_read_b128 v[138:141], v39 offset:5120
	s_waitcnt lgkmcnt(11)
	v_pk_mul_f32 v[210:211], v[94:95], v[142:143]
	v_pk_fma_f32 v[210:211], v[92:93], v[144:145], v[210:211]
	ds_read_b128 v[142:145], v39 offset:9216
	s_waitcnt lgkmcnt(11)
	v_pk_mul_f32 v[212:213], v[94:95], v[146:147]
	v_pk_fma_f32 v[212:213], v[92:93], v[148:149], v[212:213]
	ds_read_b128 v[146:149], v39 offset:13312
	s_waitcnt lgkmcnt(11)
	v_pk_mul_f32 v[184:185], v[94:95], v[232:233]
	v_pk_fma_f32 v[184:185], v[92:93], v[234:235], v[184:185]
	ds_read_b128 v[232:235], v39 offset:17408
	s_waitcnt lgkmcnt(11)
	v_pk_mul_f32 v[186:187], v[94:95], v[236:237]
	v_pk_fma_f32 v[186:187], v[92:93], v[238:239], v[186:187]
	ds_read_b128 v[236:239], v39 offset:21504
	s_waitcnt lgkmcnt(11)
	v_pk_mul_f32 v[188:189], v[94:95], v[240:241]
	v_pk_fma_f32 v[188:189], v[92:93], v[242:243], v[188:189]
	ds_read_b128 v[240:243], v39 offset:25600
	s_waitcnt lgkmcnt(11)
	v_pk_mul_f32 v[194:195], v[94:95], v[244:245]
	v_pk_fma_f32 v[194:195], v[92:93], v[246:247], v[194:195]
	ds_read_b128 v[244:247], v39 offset:29696
	s_waitcnt lgkmcnt(11)
	v_pk_mul_f32 v[150:151], v[94:95], v[118:119]
	v_pk_fma_f32 v[150:151], v[92:93], v[120:121], v[150:151]
	ds_read_b128 v[118:121], v39 offset:33792
	s_waitcnt lgkmcnt(11)
	v_pk_mul_f32 v[224:225], v[94:95], v[122:123]
	v_pk_fma_f32 v[224:225], v[92:93], v[124:125], v[224:225]
	ds_read_b128 v[122:125], v39 offset:37888
	s_waitcnt lgkmcnt(11)
	v_pk_mul_f32 v[230:231], v[94:95], v[126:127]
	v_pk_fma_f32 v[230:231], v[92:93], v[128:129], v[230:231]
	ds_read_b128 v[126:129], v39 offset:41984
	s_waitcnt lgkmcnt(11)
	v_pk_mul_f32 v[88:89], v[94:95], v[130:131]
	v_pk_fma_f32 v[88:89], v[92:93], v[132:133], v[88:89]
	ds_read_b128 v[130:133], v39 offset:46080
	s_waitcnt lgkmcnt(11)
	v_pk_fma_f32 v[196:197], v[70:71], v[134:135], v[196:197]
	v_pk_fma_f32 v[196:197], v[68:69], v[136:137], v[196:197]
	ds_read_b128 v[134:137], v39 offset:50176
	s_waitcnt lgkmcnt(11)
	v_pk_fma_f32 v[198:199], v[70:71], v[138:139], v[198:199]
	v_pk_fma_f32 v[198:199], v[68:69], v[140:141], v[198:199]
	ds_read_b128 v[138:141], v39 offset:54272
	s_waitcnt lgkmcnt(11)
	v_pk_fma_f32 v[200:201], v[70:71], v[142:143], v[200:201]
	v_pk_fma_f32 v[200:201], v[68:69], v[144:145], v[200:201]
	ds_read_b128 v[142:145], v39 offset:58368
	s_waitcnt lgkmcnt(11)
	v_pk_fma_f32 v[202:203], v[70:71], v[146:147], v[202:203]
	v_pk_fma_f32 v[202:203], v[68:69], v[148:149], v[202:203]
	ds_read_b128 v[146:149], v39 offset:62464
	s_waitcnt lgkmcnt(11)
	v_pk_fma_f32 v[206:207], v[70:71], v[232:233], v[206:207]
	v_pk_fma_f32 v[206:207], v[68:69], v[234:235], v[206:207]
	ds_read_b128 v[232:235], v39 offset:2048
	s_waitcnt lgkmcnt(11)
	v_pk_fma_f32 v[208:209], v[70:71], v[236:237], v[208:209]
	v_pk_fma_f32 v[208:209], v[68:69], v[238:239], v[208:209]
	ds_read_b128 v[236:239], v39 offset:6144
	s_waitcnt lgkmcnt(11)
	v_pk_fma_f32 v[210:211], v[70:71], v[240:241], v[210:211]
	v_pk_fma_f32 v[210:211], v[68:69], v[242:243], v[210:211]
	ds_read_b128 v[240:243], v39 offset:10240
	s_waitcnt lgkmcnt(11)
	v_pk_fma_f32 v[212:213], v[70:71], v[244:245], v[212:213]
	v_pk_fma_f32 v[212:213], v[68:69], v[246:247], v[212:213]
	ds_read_b128 v[244:247], v39 offset:14336
	s_waitcnt lgkmcnt(11)
	v_pk_fma_f32 v[184:185], v[70:71], v[118:119], v[184:185]
	v_pk_fma_f32 v[184:185], v[68:69], v[120:121], v[184:185]
	ds_read_b128 v[118:121], v39 offset:18432
	s_waitcnt lgkmcnt(11)
	v_pk_fma_f32 v[186:187], v[70:71], v[122:123], v[186:187]
	v_pk_fma_f32 v[186:187], v[68:69], v[124:125], v[186:187]
	ds_read_b128 v[122:125], v39 offset:22528
	s_waitcnt lgkmcnt(11)
	v_pk_fma_f32 v[188:189], v[70:71], v[126:127], v[188:189]
	v_pk_fma_f32 v[188:189], v[68:69], v[128:129], v[188:189]
	ds_read_b128 v[126:129], v39 offset:26624
	s_waitcnt lgkmcnt(11)
	v_pk_fma_f32 v[194:195], v[70:71], v[130:131], v[194:195]
	v_pk_fma_f32 v[194:195], v[68:69], v[132:133], v[194:195]
	ds_read_b128 v[130:133], v39 offset:30720
	s_waitcnt lgkmcnt(11)
	v_pk_fma_f32 v[150:151], v[70:71], v[134:135], v[150:151]
	v_pk_fma_f32 v[150:151], v[68:69], v[136:137], v[150:151]
	ds_read_b128 v[134:137], v39 offset:34816
	s_waitcnt lgkmcnt(11)
	v_pk_fma_f32 v[224:225], v[70:71], v[138:139], v[224:225]
	v_pk_fma_f32 v[224:225], v[68:69], v[140:141], v[224:225]
	ds_read_b128 v[138:141], v39 offset:38912
	s_waitcnt lgkmcnt(11)
	v_pk_fma_f32 v[230:231], v[70:71], v[142:143], v[230:231]
	v_pk_fma_f32 v[230:231], v[68:69], v[144:145], v[230:231]
	ds_read_b128 v[142:145], v39 offset:43008
	s_waitcnt lgkmcnt(11)
	v_pk_fma_f32 v[88:89], v[70:71], v[146:147], v[88:89]
	v_pk_fma_f32 v[88:89], v[68:69], v[148:149], v[88:89]
	ds_read_b128 v[146:149], v39 offset:47104
	s_waitcnt lgkmcnt(11)
; #define LAS __attribute__((address_space(3)))
; __device__ __forceinline__ void ph_ln1(const Params& p, int l, LAS unsigned char* lds, const int wvid) {
;     ...
;         for (int j = 0; j < 4; ++j)
; #pragma unroll
;             for (int e = 0; e < 16; ++e) { const f32x4 w = *(const LAS f32x4*)(rw + e * D + 256 * j + 4 * lane);
;                 lg[e] += (v[j][0] * w[0] + v[j][1] * w[1]) + (v[j][2] * w[2] + v[j][3] * w[3]); }
	v_pk_fma_f32 v[196:197], v[66:67], v[232:233], v[196:197]
	v_pk_fma_f32 v[196:197], v[64:65], v[234:235], v[196:197]
	ds_read_b128 v[232:235], v39 offset:51200
	s_waitcnt lgkmcnt(11)
	v_pk_fma_f32 v[198:199], v[66:67], v[236:237], v[198:199]
	v_pk_fma_f32 v[198:199], v[64:65], v[238:239], v[198:199]
	ds_read_b128 v[236:239], v39 offset:55296
	s_waitcnt lgkmcnt(11)
	v_pk_fma_f32 v[200:201], v[66:67], v[240:241], v[200:201]
	v_pk_fma_f32 v[200:201], v[64:65], v[242:243], v[200:201]
	ds_read_b128 v[240:243], v39 offset:59392
	s_waitcnt lgkmcnt(11)
	v_pk_fma_f32 v[202:203], v[66:67], v[244:245], v[202:203]
	v_pk_fma_f32 v[202:203], v[64:65], v[246:247], v[202:203]
	ds_read_b128 v[244:247], v39 offset:63488
	s_waitcnt lgkmcnt(11)
	v_pk_fma_f32 v[206:207], v[66:67], v[118:119], v[206:207]
	v_pk_fma_f32 v[206:207], v[64:65], v[120:121], v[206:207]
	ds_read_b128 v[118:121], v39 offset:3072
	s_waitcnt lgkmcnt(11)
	v_pk_fma_f32 v[208:209], v[66:67], v[122:123], v[208:209]
	v_pk_fma_f32 v[208:209], v[64:65], v[124:125], v[208:209]
	ds_read_b128 v[122:125], v39 offset:7168
	s_waitcnt lgkmcnt(11)
	v_pk_fma_f32 v[210:211], v[66:67], v[126:127], v[210:211]
	v_pk_fma_f32 v[210:211], v[64:65], v[128:129], v[210:211]
	ds_read_b128 v[126:129], v39 offset:11264
	s_waitcnt lgkmcnt(11)
	v_pk_fma_f32 v[212:213], v[66:67], v[130:131], v[212:213]
	v_pk_fma_f32 v[212:213], v[64:65], v[132:133], v[212:213]
	ds_read_b128 v[130:133], v39 offset:15360
	s_waitcnt lgkmcnt(11)
	v_pk_fma_f32 v[184:185], v[66:67], v[134:135], v[184:185]
	v_pk_fma_f32 v[184:185], v[64:65], v[136:137], v[184:185]
	ds_read_b128 v[134:137], v39 offset:19456
	s_waitcnt lgkmcnt(11)
	v_pk_fma_f32 v[186:187], v[66:67], v[138:139], v[186:187]
	v_pk_fma_f32 v[186:187], v[64:65], v[140:141], v[186:187]
	ds_read_b128 v[138:141], v39 offset:23552
	s_waitcnt lgkmcnt(11)
	v_pk_fma_f32 v[188:189], v[66:67], v[142:143], v[188:189]
	v_pk_fma_f32 v[188:189], v[64:65], v[144:145], v[188:189]
	ds_read_b128 v[142:145], v39 offset:27648
	s_waitcnt lgkmcnt(11)
	v_pk_fma_f32 v[194:195], v[66:67], v[146:147], v[194:195]
	v_pk_fma_f32 v[194:195], v[64:65], v[148:149], v[194:195]
	ds_read_b128 v[146:149], v39 offset:31744
	s_waitcnt lgkmcnt(11)
	v_pk_fma_f32 v[150:151], v[66:67], v[232:233], v[150:151]
	v_pk_fma_f32 v[150:151], v[64:65], v[234:235], v[150:151]
	ds_read_b128 v[232:235], v39 offset:35840
	s_waitcnt lgkmcnt(11)
	v_pk_fma_f32 v[224:225], v[66:67], v[236:237], v[224:225]
	v_pk_fma_f32 v[224:225], v[64:65], v[238:239], v[224:225]
	ds_read_b128 v[236:239], v39 offset:39936
	s_waitcnt lgkmcnt(11)
	v_pk_fma_f32 v[230:231], v[66:67], v[240:241], v[230:231]
	v_pk_fma_f32 v[230:231], v[64:65], v[242:243], v[230:231]
	ds_read_b128 v[240:243], v39 offset:44032
	s_waitcnt lgkmcnt(11)
	v_pk_fma_f32 v[88:89], v[66:67], v[244:245], v[88:89]
	v_pk_fma_f32 v[88:89], v[64:65], v[246:247], v[88:89]
	ds_read_b128 v[244:247], v39 offset:48128
	s_waitcnt lgkmcnt(11)
	v_pk_fma_f32 v[196:197], v[62:63], v[118:119], v[196:197]
	v_pk_fma_f32 v[196:197], v[60:61], v[120:121], v[196:197]
	ds_read_b128 v[118:121], v39 offset:52224
	s_waitcnt lgkmcnt(11)
	v_pk_fma_f32 v[198:199], v[62:63], v[122:123], v[198:199]
	v_pk_fma_f32 v[198:199], v[60:61], v[124:125], v[198:199]
	ds_read_b128 v[122:125], v39 offset:56320
	s_waitcnt lgkmcnt(11)
	v_pk_fma_f32 v[200:201], v[62:63], v[126:127], v[200:201]
	v_pk_fma_f32 v[200:201], v[60:61], v[128:129], v[200:201]
	ds_read_b128 v[126:129], v39 offset:60416
	s_waitcnt lgkmcnt(11)
	v_pk_fma_f32 v[202:203], v[62:63], v[130:131], v[202:203]
	v_pk_fma_f32 v[202:203], v[60:61], v[132:133], v[202:203]
	ds_read_b128 v[130:133], v39 offset:64512
	s_waitcnt lgkmcnt(11)
	v_pk_fma_f32 v[206:207], v[62:63], v[134:135], v[206:207]
	v_pk_fma_f32 v[206:207], v[60:61], v[136:137], v[206:207]
	s_waitcnt lgkmcnt(10)
	v_pk_fma_f32 v[208:209], v[62:63], v[138:139], v[208:209]
	v_pk_fma_f32 v[208:209], v[60:61], v[140:141], v[208:209]
	s_waitcnt lgkmcnt(9)
	v_pk_fma_f32 v[210:211], v[62:63], v[142:143], v[210:211]
	v_pk_fma_f32 v[210:211], v[60:61], v[144:145], v[210:211]
	s_waitcnt lgkmcnt(8)
	v_pk_fma_f32 v[212:213], v[62:63], v[146:147], v[212:213]
	v_pk_fma_f32 v[212:213], v[60:61], v[148:149], v[212:213]
	s_waitcnt lgkmcnt(7)
; #define LAS __attribute__((address_space(3)))
; template <int CTRL> __device__ __forceinline__ float dpp_get(float v) { return __int_as_float(__builtin_amdgcn_update_dpp(0, __float_as_int(v), CTRL, 0xF, 0xF, false)); }
; __device__ __forceinline__ void ph_ln1(const Params& p, int l, LAS unsigned char* lds, const int wvid) {
;     ...
;         for (int j = 0; j < 4; ++j)
; #pragma unroll
;             for (int e = 0; e < 16; ++e) { const f32x4 w = *(const LAS f32x4*)(rw + e * D + 256 * j + 4 * lane);
;                 lg[e] += (v[j][0] * w[0] + v[j][1] * w[1]) + (v[j][2] * w[2] + v[j][3] * w[3]); }
;         { const bool b3 = lane & 8, b2 = lane & 4, b1 = lane & 2, b0 = lane & 1;
;           float h8[8], h4[4], h2[2];
; #pragma unroll
;           for (int i = 0; i < 8; ++i) h8[i] = (b3 ? lg[i + 8] : lg[i]) + dpp_get<0x128>(b3 ? lg[i] : lg[i + 8]);
; #pragma unroll
;           for (int i = 0; i < 4; ++i) h4[i] = (b2 ? h8[i + 4] : h8[i]) + dpp_get<0x141>(b2 ? h8[i] : h8[i + 4]);
; #pragma unroll
;           for (int i = 0; i < 2; ++i) h2[i] = (b1 ? h4[i + 2] : h4[i]) + dpp_get<0x4E>(b1 ? h4[i] : h4[i + 2]);
;           float x = (b0 ? h2[1] : h2[0]) + dpp_get<0xB1>(b0 ? h2[0] : h2[1]);
;           x += __shfl_xor(x, 16); x += __shfl_xor(x, 32);
;           if (lane < 16) LG[(wave * 20 + k) * 16 + lane] = x; }
	v_pk_fma_f32 v[184:185], v[62:63], v[232:233], v[184:185]
	v_pk_fma_f32 v[184:185], v[60:61], v[234:235], v[184:185]
	s_waitcnt lgkmcnt(6)
	v_pk_fma_f32 v[186:187], v[62:63], v[236:237], v[186:187]
	v_pk_fma_f32 v[186:187], v[60:61], v[238:239], v[186:187]
	s_waitcnt lgkmcnt(5)
	v_pk_fma_f32 v[188:189], v[62:63], v[240:241], v[188:189]
	v_pk_fma_f32 v[188:189], v[60:61], v[242:243], v[188:189]
	s_waitcnt lgkmcnt(4)
	v_pk_fma_f32 v[194:195], v[62:63], v[244:245], v[194:195]
	v_pk_fma_f32 v[194:195], v[60:61], v[246:247], v[194:195]
	s_waitcnt lgkmcnt(3)
	v_pk_fma_f32 v[150:151], v[62:63], v[118:119], v[150:151]
	v_pk_fma_f32 v[150:151], v[60:61], v[120:121], v[150:151]
	s_waitcnt lgkmcnt(2)
	v_pk_fma_f32 v[224:225], v[62:63], v[122:123], v[224:225]
	v_pk_fma_f32 v[224:225], v[60:61], v[124:125], v[224:225]
	s_waitcnt lgkmcnt(1)
	v_pk_fma_f32 v[230:231], v[62:63], v[126:127], v[230:231]
	v_pk_fma_f32 v[230:231], v[60:61], v[128:129], v[230:231]
	s_waitcnt lgkmcnt(0)
	v_pk_fma_f32 v[88:89], v[62:63], v[130:131], v[88:89]
	v_pk_fma_f32 v[88:89], v[60:61], v[132:133], v[88:89]
	v_add_f32_e32 v64, v196, v197
	v_add_f32_e32 v65, v198, v199
	v_add_f32_e32 v66, v200, v201
	v_add_f32_e32 v67, v202, v203
	v_add_f32_e32 v72, v206, v207
	v_add_f32_e32 v74, v208, v209
	v_add_f32_e32 v73, v210, v211
	v_add_f32_e32 v71, v212, v213
	v_add_f32_e32 v70, v184, v185
	v_add_f32_e32 v69, v186, v187
	v_add_f32_e32 v68, v188, v189
	v_add_f32_e32 v75, v194, v195
	v_add_f32_e32 v80, v150, v151
	v_add_f32_e32 v81, v224, v225
	v_add_f32_e32 v76, v230, v231
	v_add_f32_e32 v0, v88, v89
	v_cndmask_b32_e32 v34, v70, v64, vcc
	v_cndmask_b32_e32 v35, v64, v70, vcc
	v_cndmask_b32_e32 v36, v65, v69, vcc
	v_cndmask_b32_e32 v37, v66, v68, vcc
	v_add_f32_dpp v34, v35, v34 row_ror:8 row_mask:0xf bank_mask:0xf bound_ctrl:1
	v_cndmask_b32_e32 v35, v69, v65, vcc
	v_cndmask_b32_e32 v60, v67, v75, vcc
	v_cndmask_b32_e32 v61, v72, v80, vcc
	v_add_f32_dpp v35, v36, v35 row_ror:8 row_mask:0xf bank_mask:0xf bound_ctrl:1
	v_cndmask_b32_e32 v36, v68, v66, vcc
	v_cndmask_b32_e32 v62, v74, v81, vcc
	v_cndmask_b32_e32 v63, v73, v76, vcc
	v_add_f32_dpp v36, v37, v36 row_ror:8 row_mask:0xf bank_mask:0xf bound_ctrl:1
	v_cndmask_b32_e32 v37, v75, v67, vcc
	s_nop 1
	v_add_f32_dpp v37, v60, v37 row_ror:8 row_mask:0xf bank_mask:0xf bound_ctrl:1
	v_cndmask_b32_e32 v60, v80, v72, vcc
	s_nop 1
	v_add_f32_dpp v60, v61, v60 row_ror:8 row_mask:0xf bank_mask:0xf bound_ctrl:1
	v_cndmask_b32_e32 v61, v81, v74, vcc
	s_nop 1
	v_add_f32_dpp v61, v62, v61 row_ror:8 row_mask:0xf bank_mask:0xf bound_ctrl:1
	v_cndmask_b32_e32 v62, v76, v73, vcc
	s_nop 1
	v_add_f32_dpp v62, v63, v62 row_ror:8 row_mask:0xf bank_mask:0xf bound_ctrl:1
	v_cndmask_b32_e32 v63, v0, v71, vcc
	v_cndmask_b32_e32 v0, v71, v0, vcc
	s_nop 1
	v_add_f32_dpp v0, v0, v63 row_ror:8 row_mask:0xf bank_mask:0xf bound_ctrl:1
	v_cndmask_b32_e64 v63, v60, v34, s[4:5]
	v_cndmask_b32_e64 v34, v34, v60, s[4:5]
	v_cndmask_b32_e64 v60, v61, v35, s[4:5]
	v_cndmask_b32_e64 v35, v35, v61, s[4:5]
	v_add_f32_dpp v34, v34, v63 row_half_mirror row_mask:0xf bank_mask:0xf bound_ctrl:1
	s_nop 0
	v_add_f32_dpp v35, v35, v60 row_half_mirror row_mask:0xf bank_mask:0xf bound_ctrl:1
	v_cndmask_b32_e64 v60, v62, v36, s[4:5]
	v_cndmask_b32_e64 v36, v36, v62, s[4:5]
	s_nop 1
	v_add_f32_dpp v36, v36, v60 row_half_mirror row_mask:0xf bank_mask:0xf bound_ctrl:1
	v_cndmask_b32_e64 v60, v0, v37, s[4:5]
	v_cndmask_b32_e64 v0, v37, v0, s[4:5]
	v_cndmask_b32_e64 v37, v36, v34, s[6:7]
	v_cndmask_b32_e64 v34, v34, v36, s[6:7]
	v_add_f32_dpp v0, v0, v60 row_half_mirror row_mask:0xf bank_mask:0xf bound_ctrl:1
	v_cndmask_b32_e64 v36, v0, v35, s[6:7]
	v_cndmask_b32_e64 v0, v35, v0, s[6:7]
	v_add_f32_dpp v34, v34, v37 quad_perm:[2,3,0,1] row_mask:0xf bank_mask:0xf bound_ctrl:1
	s_nop 0
	v_add_f32_dpp v0, v0, v36 quad_perm:[2,3,0,1] row_mask:0xf bank_mask:0xf bound_ctrl:1
	v_cndmask_b32_e64 v35, v0, v34, s[8:9]
	v_cndmask_b32_e64 v0, v34, v0, s[8:9]
	s_nop 1
	v_add_f32_dpp v0, v0, v35 quad_perm:[1,0,3,2] row_mask:0xf bank_mask:0xf bound_ctrl:1
	ds_bpermute_b32 v34, v43, v0
	s_waitcnt lgkmcnt(0)
	v_add_f32_e32 v0, v0, v34
	ds_bpermute_b32 v34, v85, v0
	s_and_saveexec_b64 s[0:1], s[10:11]
	s_cbranch_execz .LBB0_1073
	s_waitcnt lgkmcnt(0)
	v_add_f32_e32 v0, v0, v34
	ds_write_b32 v86, v0
	s_branch .LBB0_1073
